# P12 v-loop: output pieces staged in dead LDS, written 8 at a time every second slice
# speedup vs baseline: 1.0129x; 1.0053x over previous
; #define P12_VISSUE(c_, i_, q_, D_X) do { _Pragma("unroll") for (int b = 0; b < 8; ++b) { const int idx = ((q_) * 8 + b) * 4 + eg; const unsigned ro = (unsigned)(c_) * 16384u + (unsigned)EL[(i_) * 128 + idx]; \
;           const v3u_ ld_ = *(const v3u_*)(V8 + (size_t)(ro * 192u + 12u * (unsigned)cl)); if (b & 1) D_X[b >> 1].hi = ld_; else D_X[b >> 1].lo = ld_; } } while (0)
; __device__ __forceinline__ void p12_peer(Frame& F) {
;     ...
;       v6u_ dA[4], dB[4];
;       P12_VISSUE(0, 0, 0, dA);
; _Pragma("nounroll")
;       for (int c = 0; c < 16; ++c) {
;           int lo_ = 16 * cl + 4 * eg; asm volatile("" : "+v"(lo_));
; _Pragma("nounroll")
;           for (int i = 0; i < 4; ++i) { const int t = F.gw + i * F.NGW;
;               f32x2 acc2[8];
; #pragma unroll
;               for (int m = 0; m < 8; ++m) acc2[m] = (f32x2){0.f, 0.f};
;               const v2u hb = *(const v2u*)(HN + ((size_t)t * D_ + (size_t)(unsigned)(256 * c + lo_)));
;               P12_VISSUE(c, i, 1, dB); asm volatile("" ::: "memory"); P12_VCOMP(i, 0, dA);
;               P12_VISSUE(c, i, 2, dA); asm volatile("" ::: "memory"); P12_VCOMP(i, 1, dB);
;               P12_VISSUE(c, i, 3, dB); asm volatile("" ::: "memory"); P12_VCOMP(i, 2, dA);
;               { const int in_ = i + 1 < 4 ? i + 1 : 0, cn_ = i + 1 < 4 ? c : (c + 1 < 16 ? c + 1 : 15); P12_VISSUE(cn_, in_, 0, dA); } asm volatile("" ::: "memory"); P12_VCOMP(i, 3, dB);
.LBB0_3403:
	v_add_u32_e32 v152, s28, v175
	ds_read_u16 v2, v152
	ds_read_u16 v3, v152 offset:8
	ds_read_u16 v4, v152 offset:16
	ds_read_u16 v5, v152 offset:24
	ds_read_u16 v6, v152 offset:32
	ds_read_u16 v7, v152 offset:40
	ds_read_u16 v8, v152 offset:48
	ds_read_u16 v9, v152 offset:56
	s_ashr_i32 s13, s12, 31
	s_lshl_b64 s[14:15], s[12:13], 13
	v_lshl_add_u64 v[0:1], v[164:165], 0, s[14:15]
	s_cmpk_eq_i32 s28, 0x300
	global_load_dwordx2 v[158:159], v[0:1], off
	s_cselect_b32 s30, 0, s23
	s_waitcnt lgkmcnt(7)
	v_add_u32_e32 v0, s21, v2
	v_lshl_add_u32 v179, s30, 1, v161
	s_waitcnt lgkmcnt(6)
	v_add_u32_e32 v2, s21, v3
	s_waitcnt lgkmcnt(5)
	v_add_u32_e32 v4, s21, v4
	s_waitcnt lgkmcnt(4)
	v_add_u32_e32 v10, s21, v5
	s_waitcnt lgkmcnt(3)
	v_add_u32_e32 v11, s21, v6
	s_waitcnt lgkmcnt(2)
	v_add_u32_e32 v12, s21, v7
	s_waitcnt lgkmcnt(1)
	v_add_u32_e32 v13, s21, v8
	s_waitcnt lgkmcnt(0)
	v_add_u32_e32 v14, s21, v9
	v_mad_u64_u32 v[0:1], s[30:31], v0, s16, v[160:161]
	v_mad_u64_u32 v[2:3], s[30:31], v2, s16, v[160:161]
	v_mad_u64_u32 v[4:5], s[30:31], v4, s16, v[160:161]
	v_mad_u64_u32 v[6:7], s[30:31], v10, s16, v[160:161]
	v_mad_u64_u32 v[8:9], s[30:31], v11, s16, v[160:161]
	v_mad_u64_u32 v[10:11], s[30:31], v12, s16, v[160:161]
	v_mad_u64_u32 v[12:13], s[30:31], v13, s16, v[160:161]
	v_mad_u64_u32 v[14:15], s[30:31], v14, s16, v[160:161]
	global_load_dwordx3 v[154:156], v0, s[2:3]
	global_load_dwordx3 v[220:222], v2, s[2:3]
	global_load_dwordx3 v[180:182], v4, s[2:3]
	global_load_dwordx3 v[224:226], v6, s[2:3]
	global_load_dwordx3 v[186:188], v8, s[2:3]
	global_load_dwordx3 v[228:230], v10, s[2:3]
	global_load_dwordx3 v[192:194], v12, s[2:3]
	global_load_dwordx3 v[232:234], v14, s[2:3]
	ds_read2_b32 v[166:167], v177 offset1:4
	ds_read2_b32 v[168:169], v177 offset0:8 offset1:12
	s_waitcnt vmcnt(10)
	ds_read2_b32 v[184:185], v177 offset0:16 offset1:20
	s_waitcnt vmcnt(9)
	ds_read2_b32 v[190:191], v177 offset0:24 offset1:28
	v_cvt_scalef32_pk32_f32_fp6 v[96:127], v[134:139], 1.0
	v_cvt_scalef32_pk32_f32_fp6 v[64:95], v[128:133], 1.0
	ds_read_u16 v129, v152 offset:64
	ds_read_u16 v131, v152 offset:72
	ds_read_u16 v132, v152 offset:80
	ds_read_u16 v133, v152 offset:88
	ds_read_u16 v134, v152 offset:96
	ds_read_u16 v135, v152 offset:104
	ds_read_u16 v136, v152 offset:112
	ds_read_u16 v137, v152 offset:120
	s_waitcnt lgkmcnt(11)
	v_pk_fma_f32 v[96:97], v[96:97], v[166:167], 0 op_sel_hi:[1,0,0]
	v_pk_fma_f32 v[98:99], v[98:99], v[166:167], 0 op_sel_hi:[1,0,0]
	v_pk_fma_f32 v[100:101], v[100:101], v[166:167], 0 op_sel_hi:[1,0,0]
	v_pk_fma_f32 v[102:103], v[102:103], v[166:167], 0 op_sel_hi:[1,0,0]
	v_pk_fma_f32 v[104:105], v[104:105], v[166:167], 0 op_sel_hi:[1,0,0]
	v_pk_fma_f32 v[106:107], v[106:107], v[166:167], 0 op_sel_hi:[1,0,0]
	v_pk_fma_f32 v[108:109], v[108:109], v[166:167], 0 op_sel_hi:[1,0,0]
	v_pk_fma_f32 v[110:111], v[110:111], v[166:167], 0 op_sel_hi:[1,0,0]
	v_mov_b32_e32 v128, v167
	s_waitcnt lgkmcnt(7)
	v_pk_fma_f32 v[96:97], v[112:113], v[128:129], v[96:97] op_sel_hi:[1,0,1]
	v_pk_fma_f32 v[98:99], v[114:115], v[128:129], v[98:99] op_sel_hi:[1,0,1]
	v_pk_fma_f32 v[100:101], v[116:117], v[128:129], v[100:101] op_sel_hi:[1,0,1]
	v_pk_fma_f32 v[102:103], v[118:119], v[128:129], v[102:103] op_sel_hi:[1,0,1]
	v_pk_fma_f32 v[104:105], v[120:121], v[128:129], v[104:105] op_sel_hi:[1,0,1]
	v_pk_fma_f32 v[106:107], v[122:123], v[128:129], v[106:107] op_sel_hi:[1,0,1]
	v_pk_fma_f32 v[108:109], v[124:125], v[128:129], v[108:109] op_sel_hi:[1,0,1]
	v_pk_fma_f32 v[110:111], v[126:127], v[128:129], v[110:111] op_sel_hi:[1,0,1]
	v_add_u32_e32 v112, s21, v129
	v_mov_b32_e32 v130, v169
	s_waitcnt lgkmcnt(6)
	v_add_u32_e32 v113, s21, v131
	s_waitcnt lgkmcnt(5)
	v_add_u32_e32 v114, s21, v132
	s_waitcnt lgkmcnt(4)
	v_add_u32_e32 v115, s21, v133
	s_waitcnt lgkmcnt(3)
	v_add_u32_e32 v116, s21, v134
	s_waitcnt lgkmcnt(2)
	v_add_u32_e32 v117, s21, v135
	s_waitcnt lgkmcnt(1)
	v_add_u32_e32 v118, s21, v136
	s_waitcnt lgkmcnt(0)
	v_add_u32_e32 v119, s21, v137
	v_pk_fma_f32 v[64:65], v[64:65], v[168:169], v[96:97] op_sel_hi:[1,0,1]
	v_pk_fma_f32 v[66:67], v[66:67], v[168:169], v[98:99] op_sel_hi:[1,0,1]
	v_pk_fma_f32 v[68:69], v[68:69], v[168:169], v[100:101] op_sel_hi:[1,0,1]
	v_pk_fma_f32 v[70:71], v[70:71], v[168:169], v[102:103] op_sel_hi:[1,0,1]
	v_pk_fma_f32 v[72:73], v[72:73], v[168:169], v[104:105] op_sel_hi:[1,0,1]
	v_pk_fma_f32 v[74:75], v[74:75], v[168:169], v[106:107] op_sel_hi:[1,0,1]
	v_pk_fma_f32 v[76:77], v[76:77], v[168:169], v[108:109] op_sel_hi:[1,0,1]
	v_pk_fma_f32 v[78:79], v[78:79], v[168:169], v[110:111] op_sel_hi:[1,0,1]
	v_mad_u64_u32 v[96:97], s[30:31], v112, s16, v[160:161]
	v_cvt_scalef32_pk32_f32_fp6 v[32:63], v[140:145], 1.0
	v_mad_u64_u32 v[98:99], s[30:31], v113, s16, v[160:161]
	v_mad_u64_u32 v[100:101], s[30:31], v114, s16, v[160:161]
	v_mad_u64_u32 v[102:103], s[30:31], v115, s16, v[160:161]
	v_mad_u64_u32 v[104:105], s[30:31], v116, s16, v[160:161]
	v_mad_u64_u32 v[106:107], s[30:31], v117, s16, v[160:161]
	v_mad_u64_u32 v[108:109], s[30:31], v118, s16, v[160:161]
	v_mad_u64_u32 v[110:111], s[30:31], v119, s16, v[160:161]
	v_pk_fma_f32 v[64:65], v[80:81], v[130:131], v[64:65] op_sel_hi:[1,0,1]
	v_pk_fma_f32 v[66:67], v[82:83], v[130:131], v[66:67] op_sel_hi:[1,0,1]
	v_pk_fma_f32 v[68:69], v[84:85], v[130:131], v[68:69] op_sel_hi:[1,0,1]
	v_pk_fma_f32 v[70:71], v[86:87], v[130:131], v[70:71] op_sel_hi:[1,0,1]
	v_pk_fma_f32 v[72:73], v[88:89], v[130:131], v[72:73] op_sel_hi:[1,0,1]
	v_pk_fma_f32 v[74:75], v[90:91], v[130:131], v[74:75] op_sel_hi:[1,0,1]
	v_pk_fma_f32 v[76:77], v[92:93], v[130:131], v[76:77] op_sel_hi:[1,0,1]
; #define P12_VISSUE(c_, i_, q_, D_X) do { _Pragma("unroll") for (int b = 0; b < 8; ++b) { const int idx = ((q_) * 8 + b) * 4 + eg; const unsigned ro = (unsigned)(c_) * 16384u + (unsigned)EL[(i_) * 128 + idx]; \
;           const v3u_ ld_ = *(const v3u_*)(V8 + (size_t)(ro * 192u + 12u * (unsigned)cl)); if (b & 1) D_X[b >> 1].hi = ld_; else D_X[b >> 1].lo = ld_; } } while (0)
; __device__ __forceinline__ void p12_peer(Frame& F) {
;     ...
;       v6u_ dA[4], dB[4];
;       P12_VISSUE(0, 0, 0, dA);
; _Pragma("nounroll")
;       for (int c = 0; c < 16; ++c) {
;           int lo_ = 16 * cl + 4 * eg; asm volatile("" : "+v"(lo_));
; _Pragma("nounroll")
;           for (int i = 0; i < 4; ++i) { const int t = F.gw + i * F.NGW;
;               f32x2 acc2[8];
; #pragma unroll
;               for (int m = 0; m < 8; ++m) acc2[m] = (f32x2){0.f, 0.f};
;               const v2u hb = *(const v2u*)(HN + ((size_t)t * D_ + (size_t)(unsigned)(256 * c + lo_)));
;               P12_VISSUE(c, i, 1, dB); asm volatile("" ::: "memory"); P12_VCOMP(i, 0, dA);
;               P12_VISSUE(c, i, 2, dA); asm volatile("" ::: "memory"); P12_VCOMP(i, 1, dB);
;               P12_VISSUE(c, i, 3, dB); asm volatile("" ::: "memory"); P12_VCOMP(i, 2, dA);
;               { const int in_ = i + 1 < 4 ? i + 1 : 0, cn_ = i + 1 < 4 ? c : (c + 1 < 16 ? c + 1 : 15); P12_VISSUE(cn_, in_, 0, dA); } asm volatile("" ::: "memory"); P12_VCOMP(i, 3, dB);
	v_pk_fma_f32 v[78:79], v[94:95], v[130:131], v[78:79] op_sel_hi:[1,0,1]
	global_load_dwordx3 v[198:200], v96, s[2:3]
	global_load_dwordx3 v[128:130], v98, s[2:3]
	global_load_dwordx3 v[204:206], v100, s[2:3]
	global_load_dwordx3 v[132:134], v102, s[2:3]
	global_load_dwordx3 v[210:212], v104, s[2:3]
	global_load_dwordx3 v[136:138], v106, s[2:3]
	global_load_dwordx3 v[216:218], v108, s[2:3]
	global_load_dwordx3 v[140:142], v110, s[2:3]
	v_mov_b32_e32 v144, v185
	v_pk_fma_f32 v[32:33], v[32:33], v[184:185], v[64:65] op_sel_hi:[1,0,1]
	v_pk_fma_f32 v[34:35], v[34:35], v[184:185], v[66:67] op_sel_hi:[1,0,1]
	v_pk_fma_f32 v[36:37], v[36:37], v[184:185], v[68:69] op_sel_hi:[1,0,1]
	v_pk_fma_f32 v[38:39], v[38:39], v[184:185], v[70:71] op_sel_hi:[1,0,1]
	v_pk_fma_f32 v[40:41], v[40:41], v[184:185], v[72:73] op_sel_hi:[1,0,1]
	v_pk_fma_f32 v[42:43], v[42:43], v[184:185], v[74:75] op_sel_hi:[1,0,1]
	v_pk_fma_f32 v[44:45], v[44:45], v[184:185], v[76:77] op_sel_hi:[1,0,1]
	v_pk_fma_f32 v[46:47], v[46:47], v[184:185], v[78:79] op_sel_hi:[1,0,1]
	v_cvt_scalef32_pk32_f32_fp6 v[0:31], v[146:151], 1.0
	v_pk_fma_f32 v[32:33], v[48:49], v[144:145], v[32:33] op_sel_hi:[1,0,1]
	v_pk_fma_f32 v[34:35], v[50:51], v[144:145], v[34:35] op_sel_hi:[1,0,1]
	v_pk_fma_f32 v[36:37], v[52:53], v[144:145], v[36:37] op_sel_hi:[1,0,1]
	v_pk_fma_f32 v[38:39], v[54:55], v[144:145], v[38:39] op_sel_hi:[1,0,1]
	v_pk_fma_f32 v[40:41], v[56:57], v[144:145], v[40:41] op_sel_hi:[1,0,1]
	v_pk_fma_f32 v[42:43], v[58:59], v[144:145], v[42:43] op_sel_hi:[1,0,1]
	v_pk_fma_f32 v[44:45], v[60:61], v[144:145], v[44:45] op_sel_hi:[1,0,1]
	v_pk_fma_f32 v[46:47], v[62:63], v[144:145], v[46:47] op_sel_hi:[1,0,1]
	s_waitcnt vmcnt(16)
	v_lshlrev_b32_e32 v167, 16, v159
	v_lshlrev_b32_e32 v166, 16, v158
	v_and_b32_e32 v169, 0xffff0000, v159
	v_and_b32_e32 v168, 0xffff0000, v158
	s_waitcnt vmcnt(14)
	v_mov_b32_e32 v157, v220
	v_mov_b32_e32 v158, v221
	v_mov_b32_e32 v159, v222
	v_mov_b32_e32 v146, v191
	v_pk_fma_f32 v[0:1], v[0:1], v[190:191], v[32:33] op_sel_hi:[1,0,1]
	v_pk_fma_f32 v[2:3], v[2:3], v[190:191], v[34:35] op_sel_hi:[1,0,1]
	v_pk_fma_f32 v[4:5], v[4:5], v[190:191], v[36:37] op_sel_hi:[1,0,1]
	v_pk_fma_f32 v[6:7], v[6:7], v[190:191], v[38:39] op_sel_hi:[1,0,1]
	v_pk_fma_f32 v[8:9], v[8:9], v[190:191], v[40:41] op_sel_hi:[1,0,1]
	v_pk_fma_f32 v[10:11], v[10:11], v[190:191], v[42:43] op_sel_hi:[1,0,1]
	v_pk_fma_f32 v[12:13], v[12:13], v[190:191], v[44:45] op_sel_hi:[1,0,1]
	v_pk_fma_f32 v[14:15], v[14:15], v[190:191], v[46:47] op_sel_hi:[1,0,1]
	s_waitcnt vmcnt(12)
	v_mov_b32_e32 v183, v224
	v_mov_b32_e32 v184, v225
	v_mov_b32_e32 v185, v226
	s_waitcnt vmcnt(10)
	v_mov_b32_e32 v189, v228
	v_mov_b32_e32 v190, v229
	v_mov_b32_e32 v191, v230
	s_waitcnt vmcnt(8)
	v_mov_b32_e32 v195, v232
	v_mov_b32_e32 v196, v233
	v_mov_b32_e32 v197, v234
	ds_read2_b32 v[220:221], v177 offset0:32 offset1:36
	ds_read2_b32 v[222:223], v177 offset0:40 offset1:44
	ds_read2_b32 v[242:243], v177 offset0:48 offset1:52
	ds_read2_b32 v[244:245], v177 offset0:56 offset1:60
	v_cvt_scalef32_pk32_f32_fp6 v[96:127], v[154:159], 1.0
	ds_read_u16 v131, v152 offset:128
	ds_read_u16 v135, v152 offset:136
	ds_read_u16 v139, v152 offset:144
	ds_read_u16 v143, v152 offset:152
	ds_read_u16 v153, v152 offset:160
	ds_read_u16 v154, v152 offset:168
	ds_read_u16 v155, v152 offset:176
	ds_read_u16 v152, v152 offset:184
	v_pk_fma_f32 v[144:145], v[16:17], v[146:147], v[0:1] op_sel_hi:[1,0,1]
	v_pk_fma_f32 v[148:149], v[18:19], v[146:147], v[2:3] op_sel_hi:[1,0,1]
	v_pk_fma_f32 v[150:151], v[20:21], v[146:147], v[4:5] op_sel_hi:[1,0,1]
	v_pk_fma_f32 v[202:203], v[22:23], v[146:147], v[6:7] op_sel_hi:[1,0,1]
	v_pk_fma_f32 v[208:209], v[24:25], v[146:147], v[8:9] op_sel_hi:[1,0,1]
	v_pk_fma_f32 v[214:215], v[26:27], v[146:147], v[10:11] op_sel_hi:[1,0,1]
	v_pk_fma_f32 v[236:237], v[28:29], v[146:147], v[12:13] op_sel_hi:[1,0,1]
	v_pk_fma_f32 v[146:147], v[30:31], v[146:147], v[14:15] op_sel_hi:[1,0,1]
	s_waitcnt lgkmcnt(11)
	v_pk_fma_f32 v[96:97], v[96:97], v[220:221], v[144:145] op_sel_hi:[1,0,1]
	v_mov_b32_e32 v144, v221
	v_cvt_scalef32_pk32_f32_fp6 v[64:95], v[180:185], 1.0
	v_pk_fma_f32 v[98:99], v[98:99], v[220:221], v[148:149] op_sel_hi:[1,0,1]
	v_pk_fma_f32 v[100:101], v[100:101], v[220:221], v[150:151] op_sel_hi:[1,0,1]
	v_pk_fma_f32 v[102:103], v[102:103], v[220:221], v[202:203] op_sel_hi:[1,0,1]
	v_pk_fma_f32 v[104:105], v[104:105], v[220:221], v[208:209] op_sel_hi:[1,0,1]
	v_pk_fma_f32 v[106:107], v[106:107], v[220:221], v[214:215] op_sel_hi:[1,0,1]
	v_pk_fma_f32 v[108:109], v[108:109], v[220:221], v[236:237] op_sel_hi:[1,0,1]
	v_pk_fma_f32 v[110:111], v[110:111], v[220:221], v[146:147] op_sel_hi:[1,0,1]
	v_pk_fma_f32 v[96:97], v[112:113], v[144:145], v[96:97] op_sel_hi:[1,0,1]
	s_waitcnt lgkmcnt(7)
	v_add_u32_e32 v112, s21, v131
	v_pk_fma_f32 v[98:99], v[114:115], v[144:145], v[98:99] op_sel_hi:[1,0,1]
	v_pk_fma_f32 v[100:101], v[116:117], v[144:145], v[100:101] op_sel_hi:[1,0,1]
	v_pk_fma_f32 v[102:103], v[118:119], v[144:145], v[102:103] op_sel_hi:[1,0,1]
	v_pk_fma_f32 v[104:105], v[120:121], v[144:145], v[104:105] op_sel_hi:[1,0,1]
	v_pk_fma_f32 v[106:107], v[122:123], v[144:145], v[106:107] op_sel_hi:[1,0,1]
	v_pk_fma_f32 v[108:109], v[124:125], v[144:145], v[108:109] op_sel_hi:[1,0,1]
	v_pk_fma_f32 v[110:111], v[126:127], v[144:145], v[110:111] op_sel_hi:[1,0,1]
	s_waitcnt lgkmcnt(6)
	v_add_u32_e32 v113, s21, v135
	s_waitcnt lgkmcnt(5)
	v_add_u32_e32 v114, s21, v139
	s_waitcnt lgkmcnt(4)
	v_add_u32_e32 v115, s21, v143
	s_waitcnt lgkmcnt(3)
	v_add_u32_e32 v116, s21, v153
	s_waitcnt lgkmcnt(2)
; #define P12_VISSUE(c_, i_, q_, D_X) do { _Pragma("unroll") for (int b = 0; b < 8; ++b) { const int idx = ((q_) * 8 + b) * 4 + eg; const unsigned ro = (unsigned)(c_) * 16384u + (unsigned)EL[(i_) * 128 + idx]; \
;           const v3u_ ld_ = *(const v3u_*)(V8 + (size_t)(ro * 192u + 12u * (unsigned)cl)); if (b & 1) D_X[b >> 1].hi = ld_; else D_X[b >> 1].lo = ld_; } } while (0)
; __device__ __forceinline__ void p12_peer(Frame& F) {
;     ...
;       v6u_ dA[4], dB[4];
;       P12_VISSUE(0, 0, 0, dA);
; _Pragma("nounroll")
;       for (int c = 0; c < 16; ++c) {
;           int lo_ = 16 * cl + 4 * eg; asm volatile("" : "+v"(lo_));
; _Pragma("nounroll")
;           for (int i = 0; i < 4; ++i) { const int t = F.gw + i * F.NGW;
;               f32x2 acc2[8];
; #pragma unroll
;               for (int m = 0; m < 8; ++m) acc2[m] = (f32x2){0.f, 0.f};
;               const v2u hb = *(const v2u*)(HN + ((size_t)t * D_ + (size_t)(unsigned)(256 * c + lo_)));
;               P12_VISSUE(c, i, 1, dB); asm volatile("" ::: "memory"); P12_VCOMP(i, 0, dA);
;               P12_VISSUE(c, i, 2, dA); asm volatile("" ::: "memory"); P12_VCOMP(i, 1, dB);
;               P12_VISSUE(c, i, 3, dB); asm volatile("" ::: "memory"); P12_VCOMP(i, 2, dA);
;               { const int in_ = i + 1 < 4 ? i + 1 : 0, cn_ = i + 1 < 4 ? c : (c + 1 < 16 ? c + 1 : 15); P12_VISSUE(cn_, in_, 0, dA); } asm volatile("" ::: "memory"); P12_VCOMP(i, 3, dB);
	v_add_u32_e32 v117, s21, v154
	s_waitcnt lgkmcnt(1)
	v_add_u32_e32 v118, s21, v155
	s_waitcnt lgkmcnt(0)
	v_add_u32_e32 v119, s21, v152
	v_pk_fma_f32 v[64:65], v[64:65], v[222:223], v[96:97] op_sel_hi:[1,0,1]
	v_mad_u64_u32 v[96:97], s[30:31], v112, s16, v[160:161]
	v_cvt_scalef32_pk32_f32_fp6 v[32:63], v[186:191], 1.0
	v_cvt_scalef32_pk32_f32_fp6 v[0:31], v[192:197], 1.0
	v_mov_b32_e32 v146, v223
	v_pk_fma_f32 v[66:67], v[66:67], v[222:223], v[98:99] op_sel_hi:[1,0,1]
	v_pk_fma_f32 v[68:69], v[68:69], v[222:223], v[100:101] op_sel_hi:[1,0,1]
	v_pk_fma_f32 v[70:71], v[70:71], v[222:223], v[102:103] op_sel_hi:[1,0,1]
	v_pk_fma_f32 v[72:73], v[72:73], v[222:223], v[104:105] op_sel_hi:[1,0,1]
	v_pk_fma_f32 v[74:75], v[74:75], v[222:223], v[106:107] op_sel_hi:[1,0,1]
	v_pk_fma_f32 v[76:77], v[76:77], v[222:223], v[108:109] op_sel_hi:[1,0,1]
	v_pk_fma_f32 v[78:79], v[78:79], v[222:223], v[110:111] op_sel_hi:[1,0,1]
	v_mad_u64_u32 v[98:99], s[30:31], v113, s16, v[160:161]
	v_mad_u64_u32 v[100:101], s[30:31], v114, s16, v[160:161]
	v_mad_u64_u32 v[102:103], s[30:31], v115, s16, v[160:161]
	v_mad_u64_u32 v[104:105], s[30:31], v116, s16, v[160:161]
	v_mad_u64_u32 v[106:107], s[30:31], v117, s16, v[160:161]
	v_mad_u64_u32 v[108:109], s[30:31], v118, s16, v[160:161]
	v_mad_u64_u32 v[110:111], s[30:31], v119, s16, v[160:161]
	global_load_dwordx3 v[180:182], v96, s[2:3]
	global_load_dwordx3 v[226:228], v98, s[2:3]
	global_load_dwordx3 v[186:188], v100, s[2:3]
	global_load_dwordx3 v[230:232], v102, s[2:3]
	global_load_dwordx3 v[192:194], v104, s[2:3]
	global_load_dwordx3 v[234:236], v106, s[2:3]
	global_load_dwordx3 v[222:224], v108, s[2:3]
	global_load_dwordx3 v[238:240], v110, s[2:3]
	s_waitcnt vmcnt(14)
	v_mov_b32_e32 v201, v128
	v_mov_b32_e32 v202, v129
	v_mov_b32_e32 v203, v130
	s_waitcnt vmcnt(12)
	v_mov_b32_e32 v207, v132
	v_mov_b32_e32 v208, v133
	v_mov_b32_e32 v209, v134
	s_waitcnt vmcnt(10)
	v_mov_b32_e32 v213, v136
	v_mov_b32_e32 v214, v137
	v_mov_b32_e32 v215, v138
	s_waitcnt vmcnt(8)
	v_mov_b32_e32 v219, v140
	v_mov_b32_e32 v220, v141
	v_mov_b32_e32 v221, v142
	v_pk_fma_f32 v[64:65], v[80:81], v[146:147], v[64:65] op_sel_hi:[1,0,1]
	v_pk_fma_f32 v[66:67], v[82:83], v[146:147], v[66:67] op_sel_hi:[1,0,1]
	v_pk_fma_f32 v[68:69], v[84:85], v[146:147], v[68:69] op_sel_hi:[1,0,1]
	v_pk_fma_f32 v[70:71], v[86:87], v[146:147], v[70:71] op_sel_hi:[1,0,1]
	v_pk_fma_f32 v[72:73], v[88:89], v[146:147], v[72:73] op_sel_hi:[1,0,1]
	v_pk_fma_f32 v[74:75], v[90:91], v[146:147], v[74:75] op_sel_hi:[1,0,1]
	v_pk_fma_f32 v[76:77], v[92:93], v[146:147], v[76:77] op_sel_hi:[1,0,1]
	v_pk_fma_f32 v[78:79], v[94:95], v[146:147], v[78:79] op_sel_hi:[1,0,1]
	ds_read2_b32 v[196:197], v177 offset0:64 offset1:68
	v_mov_b32_e32 v184, v243
	ds_read2_b32 v[246:247], v177 offset0:72 offset1:76
	ds_read2_b32 v[248:249], v177 offset0:80 offset1:84
	ds_read2_b32 v[250:251], v177 offset0:88 offset1:92
	v_pk_fma_f32 v[32:33], v[32:33], v[242:243], v[64:65] op_sel_hi:[1,0,1]
	v_pk_fma_f32 v[34:35], v[34:35], v[242:243], v[66:67] op_sel_hi:[1,0,1]
	v_pk_fma_f32 v[36:37], v[36:37], v[242:243], v[68:69] op_sel_hi:[1,0,1]
	v_pk_fma_f32 v[38:39], v[38:39], v[242:243], v[70:71] op_sel_hi:[1,0,1]
	v_pk_fma_f32 v[40:41], v[40:41], v[242:243], v[72:73] op_sel_hi:[1,0,1]
	v_pk_fma_f32 v[42:43], v[42:43], v[242:243], v[74:75] op_sel_hi:[1,0,1]
	v_pk_fma_f32 v[44:45], v[44:45], v[242:243], v[76:77] op_sel_hi:[1,0,1]
	v_pk_fma_f32 v[46:47], v[46:47], v[242:243], v[78:79] op_sel_hi:[1,0,1]
	v_cvt_scalef32_pk32_f32_fp6 v[128:159], v[198:203], 1.0
	v_cvt_scalef32_pk32_f32_fp6 v[96:127], v[204:209], 1.0
	v_cvt_scalef32_pk32_f32_fp6 v[64:95], v[210:215], 1.0
	v_pk_fma_f32 v[198:199], v[48:49], v[184:185], v[32:33] op_sel_hi:[1,0,1]
	v_pk_fma_f32 v[200:201], v[50:51], v[184:185], v[34:35] op_sel_hi:[1,0,1]
	v_pk_fma_f32 v[202:203], v[52:53], v[184:185], v[36:37] op_sel_hi:[1,0,1]
	v_pk_fma_f32 v[204:205], v[54:55], v[184:185], v[38:39] op_sel_hi:[1,0,1]
	v_pk_fma_f32 v[206:207], v[56:57], v[184:185], v[40:41] op_sel_hi:[1,0,1]
	v_pk_fma_f32 v[208:209], v[58:59], v[184:185], v[42:43] op_sel_hi:[1,0,1]
	v_pk_fma_f32 v[210:211], v[60:61], v[184:185], v[44:45] op_sel_hi:[1,0,1]
	v_pk_fma_f32 v[184:185], v[62:63], v[184:185], v[46:47] op_sel_hi:[1,0,1]
	ds_read_u16 v183, v179 offset:16384
	ds_read_u16 v189, v179 offset:16392
	ds_read_u16 v191, v179 offset:16400
	ds_read_u16 v195, v179 offset:16408
	ds_read_u16 v212, v179 offset:16416
	ds_read_u16 v213, v179 offset:16424
	ds_read_u16 v214, v179 offset:16432
	ds_read_u16 v179, v179 offset:16440
	v_mov_b32_e32 v190, v245
	v_pk_fma_f32 v[0:1], v[0:1], v[244:245], v[198:199] op_sel_hi:[1,0,1]
	v_pk_fma_f32 v[2:3], v[2:3], v[244:245], v[200:201] op_sel_hi:[1,0,1]
	v_pk_fma_f32 v[4:5], v[4:5], v[244:245], v[202:203] op_sel_hi:[1,0,1]
	v_pk_fma_f32 v[6:7], v[6:7], v[244:245], v[204:205] op_sel_hi:[1,0,1]
	v_pk_fma_f32 v[8:9], v[8:9], v[244:245], v[206:207] op_sel_hi:[1,0,1]
	v_pk_fma_f32 v[10:11], v[10:11], v[244:245], v[208:209] op_sel_hi:[1,0,1]
	v_pk_fma_f32 v[12:13], v[12:13], v[244:245], v[210:211] op_sel_hi:[1,0,1]
	v_pk_fma_f32 v[14:15], v[14:15], v[244:245], v[184:185] op_sel_hi:[1,0,1]
	s_cselect_b32 s29, s22, s17
	s_waitcnt lgkmcnt(5)
; #define P12_VISSUE(c_, i_, q_, D_X) do { _Pragma("unroll") for (int b = 0; b < 8; ++b) { const int idx = ((q_) * 8 + b) * 4 + eg; const unsigned ro = (unsigned)(c_) * 16384u + (unsigned)EL[(i_) * 128 + idx]; \
;           const v3u_ ld_ = *(const v3u_*)(V8 + (size_t)(ro * 192u + 12u * (unsigned)cl)); if (b & 1) D_X[b >> 1].hi = ld_; else D_X[b >> 1].lo = ld_; } } while (0)
; __device__ __forceinline__ void p12_peer(Frame& F) {
;     ...
;       v6u_ dA[4], dB[4];
;       P12_VISSUE(0, 0, 0, dA);
; _Pragma("nounroll")
;       for (int c = 0; c < 16; ++c) {
;           int lo_ = 16 * cl + 4 * eg; asm volatile("" : "+v"(lo_));
; _Pragma("nounroll")
;           for (int i = 0; i < 4; ++i) { const int t = F.gw + i * F.NGW;
;               f32x2 acc2[8];
; #pragma unroll
;               for (int m = 0; m < 8; ++m) acc2[m] = (f32x2){0.f, 0.f};
;               const v2u hb = *(const v2u*)(HN + ((size_t)t * D_ + (size_t)(unsigned)(256 * c + lo_)));
;               P12_VISSUE(c, i, 1, dB); asm volatile("" ::: "memory"); P12_VCOMP(i, 0, dA);
;               P12_VISSUE(c, i, 2, dA); asm volatile("" ::: "memory"); P12_VCOMP(i, 1, dB);
;               P12_VISSUE(c, i, 3, dB); asm volatile("" ::: "memory"); P12_VCOMP(i, 2, dA);
;               { const int in_ = i + 1 < 4 ? i + 1 : 0, cn_ = i + 1 < 4 ? c : (c + 1 < 16 ? c + 1 : 15); P12_VISSUE(cn_, in_, 0, dA); } asm volatile("" ::: "memory"); P12_VCOMP(i, 3, dB);
	v_pk_fma_f32 v[0:1], v[16:17], v[190:191], v[0:1] op_sel_hi:[1,0,1]
	v_pk_fma_f32 v[2:3], v[18:19], v[190:191], v[2:3] op_sel_hi:[1,0,1]
	v_pk_fma_f32 v[4:5], v[20:21], v[190:191], v[4:5] op_sel_hi:[1,0,1]
	v_pk_fma_f32 v[6:7], v[22:23], v[190:191], v[6:7] op_sel_hi:[1,0,1]
	v_pk_fma_f32 v[8:9], v[24:25], v[190:191], v[8:9] op_sel_hi:[1,0,1]
	v_pk_fma_f32 v[10:11], v[26:27], v[190:191], v[10:11] op_sel_hi:[1,0,1]
	v_pk_fma_f32 v[12:13], v[28:29], v[190:191], v[12:13] op_sel_hi:[1,0,1]
	v_pk_fma_f32 v[14:15], v[30:31], v[190:191], v[14:15] op_sel_hi:[1,0,1]
	s_lshl_b64 s[14:15], s[12:13], 14
	s_lshl_b32 s13, s29, 14
	v_pk_fma_f32 v[0:1], v[128:129], v[196:197], v[0:1] op_sel_hi:[1,0,1]
	v_pk_fma_f32 v[2:3], v[130:131], v[196:197], v[2:3] op_sel_hi:[1,0,1]
	v_pk_fma_f32 v[4:5], v[132:133], v[196:197], v[4:5] op_sel_hi:[1,0,1]
	v_pk_fma_f32 v[6:7], v[134:135], v[196:197], v[6:7] op_sel_hi:[1,0,1]
	v_pk_fma_f32 v[8:9], v[136:137], v[196:197], v[8:9] op_sel_hi:[1,0,1]
	v_pk_fma_f32 v[10:11], v[138:139], v[196:197], v[10:11] op_sel_hi:[1,0,1]
	v_pk_fma_f32 v[12:13], v[140:141], v[196:197], v[12:13] op_sel_hi:[1,0,1]
	v_pk_fma_f32 v[14:15], v[142:143], v[196:197], v[14:15] op_sel_hi:[1,0,1]
	v_mov_b32_e32 v16, v197
	v_pk_fma_f32 v[0:1], v[144:145], v[16:17], v[0:1] op_sel_hi:[1,0,1]
	v_pk_fma_f32 v[2:3], v[146:147], v[16:17], v[2:3] op_sel_hi:[1,0,1]
	v_pk_fma_f32 v[4:5], v[148:149], v[16:17], v[4:5] op_sel_hi:[1,0,1]
	v_pk_fma_f32 v[6:7], v[150:151], v[16:17], v[6:7] op_sel_hi:[1,0,1]
	v_pk_fma_f32 v[8:9], v[152:153], v[16:17], v[8:9] op_sel_hi:[1,0,1]
	v_pk_fma_f32 v[10:11], v[154:155], v[16:17], v[10:11] op_sel_hi:[1,0,1]
	v_pk_fma_f32 v[12:13], v[156:157], v[16:17], v[12:13] op_sel_hi:[1,0,1]
	v_pk_fma_f32 v[14:15], v[158:159], v[16:17], v[14:15] op_sel_hi:[1,0,1]
	v_add_u32_e32 v16, s13, v183
	v_add_u32_e32 v19, s13, v189
	v_add_u32_e32 v21, s13, v191
	s_waitcnt lgkmcnt(4)
	v_add_u32_e32 v23, s13, v195
	s_waitcnt lgkmcnt(3)
	v_add_u32_e32 v30, s13, v212
	s_waitcnt lgkmcnt(2)
	v_add_u32_e32 v128, s13, v213
	s_waitcnt lgkmcnt(1)
	v_add_u32_e32 v129, s13, v214
	s_waitcnt lgkmcnt(0)
	v_add_u32_e32 v130, s13, v179
	v_mad_u64_u32 v[16:17], s[30:31], v16, s16, v[160:161]
	v_pk_fma_f32 v[0:1], v[96:97], v[246:247], v[0:1] op_sel_hi:[1,0,1]
	v_pk_fma_f32 v[2:3], v[98:99], v[246:247], v[2:3] op_sel_hi:[1,0,1]
	v_pk_fma_f32 v[4:5], v[100:101], v[246:247], v[4:5] op_sel_hi:[1,0,1]
	v_mad_u64_u32 v[24:25], s[30:31], v19, s16, v[160:161]
	v_mad_u64_u32 v[26:27], s[30:31], v21, s16, v[160:161]
	v_mad_u64_u32 v[28:29], s[30:31], v23, s16, v[160:161]
	v_mad_u64_u32 v[30:31], s[30:31], v30, s16, v[160:161]
	v_mad_u64_u32 v[96:97], s[30:31], v128, s16, v[160:161]
	v_mad_u64_u32 v[98:99], s[30:31], v129, s16, v[160:161]
	v_mad_u64_u32 v[100:101], s[30:31], v130, s16, v[160:161]
	global_load_dwordx3 v[134:136], v16, s[2:3]
	global_load_dwordx3 v[152:154], v24, s[2:3]
	global_load_dwordx3 v[128:130], v26, s[2:3]
	global_load_dwordx3 v[156:158], v28, s[2:3]
	global_load_dwordx3 v[140:142], v30, s[2:3]
	global_load_dwordx3 v[198:200], v96, s[2:3]
	global_load_dwordx3 v[146:148], v98, s[2:3]
	global_load_dwordx3 v[202:204], v100, s[2:3]
	v_mov_b32_e32 v18, v247
	v_pk_fma_f32 v[6:7], v[102:103], v[246:247], v[6:7] op_sel_hi:[1,0,1]
	v_pk_fma_f32 v[8:9], v[104:105], v[246:247], v[8:9] op_sel_hi:[1,0,1]
	v_pk_fma_f32 v[10:11], v[106:107], v[246:247], v[10:11] op_sel_hi:[1,0,1]
	v_pk_fma_f32 v[12:13], v[108:109], v[246:247], v[12:13] op_sel_hi:[1,0,1]
	v_pk_fma_f32 v[14:15], v[110:111], v[246:247], v[14:15] op_sel_hi:[1,0,1]
	s_waitcnt vmcnt(14)
	v_mov_b32_e32 v183, v226
	v_mov_b32_e32 v184, v227
	v_mov_b32_e32 v185, v228
	v_pk_fma_f32 v[0:1], v[112:113], v[18:19], v[0:1] op_sel_hi:[1,0,1]
	v_pk_fma_f32 v[2:3], v[114:115], v[18:19], v[2:3] op_sel_hi:[1,0,1]
	v_pk_fma_f32 v[4:5], v[116:117], v[18:19], v[4:5] op_sel_hi:[1,0,1]
	v_pk_fma_f32 v[6:7], v[118:119], v[18:19], v[6:7] op_sel_hi:[1,0,1]
	v_pk_fma_f32 v[8:9], v[120:121], v[18:19], v[8:9] op_sel_hi:[1,0,1]
	v_pk_fma_f32 v[10:11], v[122:123], v[18:19], v[10:11] op_sel_hi:[1,0,1]
	v_pk_fma_f32 v[12:13], v[124:125], v[18:19], v[12:13] op_sel_hi:[1,0,1]
	v_pk_fma_f32 v[14:15], v[126:127], v[18:19], v[14:15] op_sel_hi:[1,0,1]
	ds_read2_b32 v[214:215], v177 offset0:96 offset1:100
	v_mov_b32_e32 v20, v249
	v_pk_fma_f32 v[0:1], v[64:65], v[248:249], v[0:1] op_sel_hi:[1,0,1]
	v_pk_fma_f32 v[2:3], v[66:67], v[248:249], v[2:3] op_sel_hi:[1,0,1]
	v_pk_fma_f32 v[4:5], v[68:69], v[248:249], v[4:5] op_sel_hi:[1,0,1]
	v_pk_fma_f32 v[6:7], v[70:71], v[248:249], v[6:7] op_sel_hi:[1,0,1]
	v_pk_fma_f32 v[8:9], v[72:73], v[248:249], v[8:9] op_sel_hi:[1,0,1]
	v_pk_fma_f32 v[10:11], v[74:75], v[248:249], v[10:11] op_sel_hi:[1,0,1]
	v_pk_fma_f32 v[12:13], v[76:77], v[248:249], v[12:13] op_sel_hi:[1,0,1]
	v_pk_fma_f32 v[14:15], v[78:79], v[248:249], v[14:15] op_sel_hi:[1,0,1]
	s_waitcnt vmcnt(12)
	v_mov_b32_e32 v189, v230
	v_mov_b32_e32 v190, v231
	v_mov_b32_e32 v191, v232
	v_cvt_scalef32_pk32_f32_fp6 v[32:63], v[216:221], 1.0
	v_pk_fma_f32 v[0:1], v[80:81], v[20:21], v[0:1] op_sel_hi:[1,0,1]
	v_pk_fma_f32 v[2:3], v[82:83], v[20:21], v[2:3] op_sel_hi:[1,0,1]
	v_pk_fma_f32 v[4:5], v[84:85], v[20:21], v[4:5] op_sel_hi:[1,0,1]
	v_pk_fma_f32 v[6:7], v[86:87], v[20:21], v[6:7] op_sel_hi:[1,0,1]
	v_pk_fma_f32 v[8:9], v[88:89], v[20:21], v[8:9] op_sel_hi:[1,0,1]
	v_pk_fma_f32 v[10:11], v[90:91], v[20:21], v[10:11] op_sel_hi:[1,0,1]
	v_pk_fma_f32 v[12:13], v[92:93], v[20:21], v[12:13] op_sel_hi:[1,0,1]
	v_pk_fma_f32 v[14:15], v[94:95], v[20:21], v[14:15] op_sel_hi:[1,0,1]
	ds_read2_b32 v[216:217], v177 offset0:104 offset1:108
	v_mov_b32_e32 v22, v251
	v_pk_fma_f32 v[0:1], v[32:33], v[250:251], v[0:1] op_sel_hi:[1,0,1]
	v_pk_fma_f32 v[2:3], v[34:35], v[250:251], v[2:3] op_sel_hi:[1,0,1]
	v_pk_fma_f32 v[4:5], v[36:37], v[250:251], v[4:5] op_sel_hi:[1,0,1]
	v_pk_fma_f32 v[6:7], v[38:39], v[250:251], v[6:7] op_sel_hi:[1,0,1]
	v_pk_fma_f32 v[8:9], v[40:41], v[250:251], v[8:9] op_sel_hi:[1,0,1]
	v_pk_fma_f32 v[10:11], v[42:43], v[250:251], v[10:11] op_sel_hi:[1,0,1]
	v_pk_fma_f32 v[12:13], v[44:45], v[250:251], v[12:13] op_sel_hi:[1,0,1]
	v_pk_fma_f32 v[14:15], v[46:47], v[250:251], v[14:15] op_sel_hi:[1,0,1]
	s_waitcnt vmcnt(10)
; #define P12_VISSUE(c_, i_, q_, D_X) do { _Pragma("unroll") for (int b = 0; b < 8; ++b) { const int idx = ((q_) * 8 + b) * 4 + eg; const unsigned ro = (unsigned)(c_) * 16384u + (unsigned)EL[(i_) * 128 + idx]; \
;           const v3u_ ld_ = *(const v3u_*)(V8 + (size_t)(ro * 192u + 12u * (unsigned)cl)); if (b & 1) D_X[b >> 1].hi = ld_; else D_X[b >> 1].lo = ld_; } } while (0)
; __device__ __forceinline__ void p12_peer(Frame& F) {
;     ...
;       v6u_ dA[4], dB[4];
;       P12_VISSUE(0, 0, 0, dA);
; _Pragma("nounroll")
;       for (int c = 0; c < 16; ++c) {
;           int lo_ = 16 * cl + 4 * eg; asm volatile("" : "+v"(lo_));
; _Pragma("nounroll")
;           for (int i = 0; i < 4; ++i) { const int t = F.gw + i * F.NGW;
;               f32x2 acc2[8];
; #pragma unroll
;               for (int m = 0; m < 8; ++m) acc2[m] = (f32x2){0.f, 0.f};
;               const v2u hb = *(const v2u*)(HN + ((size_t)t * D_ + (size_t)(unsigned)(256 * c + lo_)));
;               P12_VISSUE(c, i, 1, dB); asm volatile("" ::: "memory"); P12_VCOMP(i, 0, dA);
;               P12_VISSUE(c, i, 2, dA); asm volatile("" ::: "memory"); P12_VCOMP(i, 1, dB);
;               P12_VISSUE(c, i, 3, dB); asm volatile("" ::: "memory"); P12_VCOMP(i, 2, dA);
;               { const int in_ = i + 1 < 4 ? i + 1 : 0, cn_ = i + 1 < 4 ? c : (c + 1 < 16 ? c + 1 : 15); P12_VISSUE(cn_, in_, 0, dA); } asm volatile("" ::: "memory"); P12_VCOMP(i, 3, dB);
	v_mov_b32_e32 v195, v234
	v_mov_b32_e32 v196, v235
	v_mov_b32_e32 v197, v236
	v_mov_b32_e32 v162, v176
	v_pk_fma_f32 v[132:133], v[48:49], v[22:23], v[0:1] op_sel_hi:[1,0,1]
	v_pk_fma_f32 v[138:139], v[50:51], v[22:23], v[2:3] op_sel_hi:[1,0,1]
	v_pk_fma_f32 v[144:145], v[52:53], v[22:23], v[4:5] op_sel_hi:[1,0,1]
	v_pk_fma_f32 v[150:151], v[54:55], v[22:23], v[6:7] op_sel_hi:[1,0,1]
	v_pk_fma_f32 v[206:207], v[56:57], v[22:23], v[8:9] op_sel_hi:[1,0,1]
	v_pk_fma_f32 v[208:209], v[58:59], v[22:23], v[10:11] op_sel_hi:[1,0,1]
	v_pk_fma_f32 v[210:211], v[60:61], v[22:23], v[12:13] op_sel_hi:[1,0,1]
	v_pk_fma_f32 v[212:213], v[62:63], v[22:23], v[14:15] op_sel_hi:[1,0,1]
	s_waitcnt vmcnt(8)
	v_mov_b32_e32 v225, v238
	v_mov_b32_e32 v226, v239
	v_mov_b32_e32 v227, v240
	ds_read2_b32 v[218:219], v177 offset0:112 offset1:116
	v_cvt_scalef32_pk32_f32_fp6 v[96:127], v[180:185], 1.0
	s_add_u32 s14, s26, s14
	ds_read2_b32 v[220:221], v177 offset0:120 offset1:124
	s_waitcnt lgkmcnt(3)
	v_pk_fma_f32 v[96:97], v[96:97], v[214:215], v[132:133] op_sel_hi:[1,0,1]
	v_pk_fma_f32 v[98:99], v[98:99], v[214:215], v[138:139] op_sel_hi:[1,0,1]
	v_pk_fma_f32 v[100:101], v[100:101], v[214:215], v[144:145] op_sel_hi:[1,0,1]
	v_pk_fma_f32 v[102:103], v[102:103], v[214:215], v[150:151] op_sel_hi:[1,0,1]
	v_pk_fma_f32 v[104:105], v[104:105], v[214:215], v[206:207] op_sel_hi:[1,0,1]
	v_pk_fma_f32 v[106:107], v[106:107], v[214:215], v[208:209] op_sel_hi:[1,0,1]
	v_pk_fma_f32 v[108:109], v[108:109], v[214:215], v[210:211] op_sel_hi:[1,0,1]
	v_pk_fma_f32 v[110:111], v[110:111], v[214:215], v[212:213] op_sel_hi:[1,0,1]
	v_mov_b32_e32 v132, v215
	s_addc_u32 s15, s27, s15
	v_cvt_scalef32_pk32_f32_fp6 v[64:95], v[186:191], 1.0
	v_add_u32_e32 v162, s18, v162
	v_pk_fma_f32 v[96:97], v[112:113], v[132:133], v[96:97] op_sel_hi:[1,0,1]
	v_pk_fma_f32 v[98:99], v[114:115], v[132:133], v[98:99] op_sel_hi:[1,0,1]
	v_pk_fma_f32 v[100:101], v[116:117], v[132:133], v[100:101] op_sel_hi:[1,0,1]
	v_pk_fma_f32 v[102:103], v[118:119], v[132:133], v[102:103] op_sel_hi:[1,0,1]
	v_pk_fma_f32 v[104:105], v[120:121], v[132:133], v[104:105] op_sel_hi:[1,0,1]
	v_pk_fma_f32 v[106:107], v[122:123], v[132:133], v[106:107] op_sel_hi:[1,0,1]
	v_pk_fma_f32 v[108:109], v[124:125], v[132:133], v[108:109] op_sel_hi:[1,0,1]
	v_pk_fma_f32 v[110:111], v[126:127], v[132:133], v[110:111] op_sel_hi:[1,0,1]
	v_lshl_add_u64 v[180:181], v[162:163], 2, s[14:15]
	s_waitcnt lgkmcnt(2)
	v_mov_b32_e32 v162, v217
	v_pk_fma_f32 v[64:65], v[64:65], v[216:217], v[96:97] op_sel_hi:[1,0,1]
	v_pk_fma_f32 v[66:67], v[66:67], v[216:217], v[98:99] op_sel_hi:[1,0,1]
	v_pk_fma_f32 v[68:69], v[68:69], v[216:217], v[100:101] op_sel_hi:[1,0,1]
	v_pk_fma_f32 v[70:71], v[70:71], v[216:217], v[102:103] op_sel_hi:[1,0,1]
	v_pk_fma_f32 v[72:73], v[72:73], v[216:217], v[104:105] op_sel_hi:[1,0,1]
	v_pk_fma_f32 v[74:75], v[74:75], v[216:217], v[106:107] op_sel_hi:[1,0,1]
	v_pk_fma_f32 v[76:77], v[76:77], v[216:217], v[108:109] op_sel_hi:[1,0,1]
	v_pk_fma_f32 v[78:79], v[78:79], v[216:217], v[110:111] op_sel_hi:[1,0,1]
	v_cvt_scalef32_pk32_f32_fp6 v[32:63], v[192:197], 1.0
	v_pk_fma_f32 v[64:65], v[80:81], v[162:163], v[64:65] op_sel_hi:[1,0,1]
	v_pk_fma_f32 v[66:67], v[82:83], v[162:163], v[66:67] op_sel_hi:[1,0,1]
	v_pk_fma_f32 v[68:69], v[84:85], v[162:163], v[68:69] op_sel_hi:[1,0,1]
	v_pk_fma_f32 v[70:71], v[86:87], v[162:163], v[70:71] op_sel_hi:[1,0,1]
	v_pk_fma_f32 v[72:73], v[88:89], v[162:163], v[72:73] op_sel_hi:[1,0,1]
	v_pk_fma_f32 v[74:75], v[90:91], v[162:163], v[74:75] op_sel_hi:[1,0,1]
	v_pk_fma_f32 v[76:77], v[92:93], v[162:163], v[76:77] op_sel_hi:[1,0,1]
	v_pk_fma_f32 v[78:79], v[94:95], v[162:163], v[78:79] op_sel_hi:[1,0,1]
	s_waitcnt lgkmcnt(1)
	v_mov_b32_e32 v182, v219
	v_pk_fma_f32 v[32:33], v[32:33], v[218:219], v[64:65] op_sel_hi:[1,0,1]
	v_pk_fma_f32 v[34:35], v[34:35], v[218:219], v[66:67] op_sel_hi:[1,0,1]
	v_pk_fma_f32 v[36:37], v[36:37], v[218:219], v[68:69] op_sel_hi:[1,0,1]
	v_pk_fma_f32 v[38:39], v[38:39], v[218:219], v[70:71] op_sel_hi:[1,0,1]
	v_pk_fma_f32 v[40:41], v[40:41], v[218:219], v[72:73] op_sel_hi:[1,0,1]
	v_pk_fma_f32 v[42:43], v[42:43], v[218:219], v[74:75] op_sel_hi:[1,0,1]
	v_pk_fma_f32 v[44:45], v[44:45], v[218:219], v[76:77] op_sel_hi:[1,0,1]
	v_pk_fma_f32 v[46:47], v[46:47], v[218:219], v[78:79] op_sel_hi:[1,0,1]
	v_cvt_scalef32_pk32_f32_fp6 v[0:31], v[222:227], 1.0
	v_pk_fma_f32 v[32:33], v[48:49], v[182:183], v[32:33] op_sel_hi:[1,0,1]
	v_pk_fma_f32 v[34:35], v[50:51], v[182:183], v[34:35] op_sel_hi:[1,0,1]
	v_pk_fma_f32 v[36:37], v[52:53], v[182:183], v[36:37] op_sel_hi:[1,0,1]
	v_pk_fma_f32 v[38:39], v[54:55], v[182:183], v[38:39] op_sel_hi:[1,0,1]
	v_pk_fma_f32 v[40:41], v[56:57], v[182:183], v[40:41] op_sel_hi:[1,0,1]
	v_pk_fma_f32 v[42:43], v[58:59], v[182:183], v[42:43] op_sel_hi:[1,0,1]
	v_pk_fma_f32 v[44:45], v[60:61], v[182:183], v[44:45] op_sel_hi:[1,0,1]
	v_pk_fma_f32 v[46:47], v[62:63], v[182:183], v[46:47] op_sel_hi:[1,0,1]
	s_waitcnt lgkmcnt(0)
; __device__ __forceinline__ float bflo(unsigned w) { return __uint_as_float(w << 16); }
; __device__ __forceinline__ float bfhi(unsigned w) { return __uint_as_float(w & 0xffff0000u); }
; __device__ __forceinline__ void p12_peer(Frame& F) {
;     ...
;               float r8[8], r4[4];
; #pragma unroll
;               for (int m = 0; m < 8; ++m) { const float lo_v = (m & 1) ? acc2[m >> 1].y : acc2[m >> 1].x, hi_v = (m & 1) ? acc2[4 + (m >> 1)].y : acc2[4 + (m >> 1)].x;
;                   const float keep = hi5 ? hi_v : lo_v, send = hi5 ? lo_v : hi_v;
;                   r8[m] = keep + __builtin_bit_cast(float, __builtin_amdgcn_ds_bpermute((F.lane ^ 32) << 2, __builtin_bit_cast(int, send))); }
; #pragma unroll
;               for (int m = 0; m < 4; ++m) { const float keep = hi4 ? r8[4 + m] : r8[m], send = hi4 ? r8[m] : r8[4 + m];
;                   r4[m] = keep + __builtin_bit_cast(float, __builtin_amdgcn_ds_bpermute((F.lane ^ 16) << 2, __builtin_bit_cast(int, send))); }
;               int lo3_ = lo_; asm volatile("" : "+v"(lo3_));
;               const size_t col = (size_t)t * D_ + (size_t)(unsigned)(256 * c + lo3_);
;               const f32x4 o = {r4[0] + bflo(hb.x), r4[1] + bfhi(hb.x), r4[2] + bflo(hb.y), r4[3] + bfhi(hb.y)};
;               SSQ[i * 64 + F.lane] += (o.x * o.x + o.y * o.y) + (o.z * o.z + o.w * o.w);
;               *(f32x4*)(F.out + col) = o;
	v_mov_b32_e32 v184, v221
	v_pk_fma_f32 v[0:1], v[0:1], v[220:221], v[32:33] op_sel_hi:[1,0,1]
	v_pk_fma_f32 v[2:3], v[2:3], v[220:221], v[34:35] op_sel_hi:[1,0,1]
	v_pk_fma_f32 v[4:5], v[4:5], v[220:221], v[36:37] op_sel_hi:[1,0,1]
	v_pk_fma_f32 v[6:7], v[6:7], v[220:221], v[38:39] op_sel_hi:[1,0,1]
	v_pk_fma_f32 v[8:9], v[8:9], v[220:221], v[40:41] op_sel_hi:[1,0,1]
	v_pk_fma_f32 v[10:11], v[10:11], v[220:221], v[42:43] op_sel_hi:[1,0,1]
	v_pk_fma_f32 v[12:13], v[12:13], v[220:221], v[44:45] op_sel_hi:[1,0,1]
	v_pk_fma_f32 v[14:15], v[14:15], v[220:221], v[46:47] op_sel_hi:[1,0,1]
	v_pk_fma_f32 v[0:1], v[16:17], v[184:185], v[0:1] op_sel_hi:[1,0,1]
	v_pk_fma_f32 v[2:3], v[18:19], v[184:185], v[2:3] op_sel_hi:[1,0,1]
	v_pk_fma_f32 v[4:5], v[20:21], v[184:185], v[4:5] op_sel_hi:[1,0,1]
	v_pk_fma_f32 v[6:7], v[22:23], v[184:185], v[6:7] op_sel_hi:[1,0,1]
	v_pk_fma_f32 v[8:9], v[24:25], v[184:185], v[8:9] op_sel_hi:[1,0,1]
	v_pk_fma_f32 v[10:11], v[26:27], v[184:185], v[10:11] op_sel_hi:[1,0,1]
	v_pk_fma_f32 v[12:13], v[28:29], v[184:185], v[12:13] op_sel_hi:[1,0,1]
	v_pk_fma_f32 v[14:15], v[30:31], v[184:185], v[14:15] op_sel_hi:[1,0,1]
	v_cndmask_b32_e32 v18, v0, v8, vcc
	v_cndmask_b32_e32 v19, v1, v9, vcc
	v_cndmask_b32_e32 v20, v2, v10, vcc
	v_cndmask_b32_e32 v21, v3, v11, vcc
	v_cndmask_b32_e32 v22, v4, v12, vcc
	v_cndmask_b32_e32 v23, v5, v13, vcc
	v_cndmask_b32_e32 v24, v6, v14, vcc
	v_cndmask_b32_e32 v25, v7, v15, vcc
	v_cndmask_b32_e32 v17, v10, v2, vcc
	v_cndmask_b32_e32 v16, v8, v0, vcc
	v_cndmask_b32_e32 v3, v11, v3, vcc
	v_cndmask_b32_e32 v2, v9, v1, vcc
	v_cndmask_b32_e32 v1, v14, v6, vcc
	v_cndmask_b32_e32 v0, v12, v4, vcc
	v_cndmask_b32_e32 v6, v13, v5, vcc
	ds_bpermute_b32 v4, v171, v18
	ds_bpermute_b32 v8, v171, v19
	ds_bpermute_b32 v5, v171, v20
	ds_bpermute_b32 v9, v171, v21
	ds_bpermute_b32 v10, v171, v22
	ds_bpermute_b32 v12, v171, v23
	ds_bpermute_b32 v11, v171, v24
	ds_bpermute_b32 v13, v171, v25
	v_cndmask_b32_e32 v7, v15, v7, vcc
	s_waitcnt lgkmcnt(5)
	v_pk_add_f32 v[4:5], v[16:17], v[4:5]
	s_waitcnt lgkmcnt(4)
	v_pk_add_f32 v[2:3], v[2:3], v[8:9]
	s_waitcnt lgkmcnt(1)
	v_pk_add_f32 v[0:1], v[0:1], v[10:11]
	s_waitcnt lgkmcnt(0)
	v_pk_add_f32 v[6:7], v[6:7], v[12:13]
	v_cndmask_b32_e64 v10, v4, v0, s[0:1]
	v_cndmask_b32_e64 v11, v2, v6, s[0:1]
	v_cndmask_b32_e64 v9, v1, v5, s[0:1]
	v_cndmask_b32_e64 v8, v0, v4, s[0:1]
	v_cndmask_b32_e64 v5, v5, v1, s[0:1]
	v_cndmask_b32_e64 v0, v6, v2, s[0:1]
	v_cndmask_b32_e64 v6, v3, v7, s[0:1]
	v_cndmask_b32_e64 v1, v7, v3, s[0:1]
	ds_bpermute_b32 v2, v170, v10
	ds_bpermute_b32 v4, v170, v11
	ds_bpermute_b32 v3, v170, v5
	ds_bpermute_b32 v5, v170, v6
	v_add_u32_e32 v178, s28, v174
	ds_read_b32 v155, v178
	s_addk_i32 s28, 0x100
	s_waitcnt lgkmcnt(2)
	v_pk_add_f32 v[2:3], v[8:9], v[2:3]
	s_waitcnt lgkmcnt(1)
	v_pk_add_f32 v[0:1], v[0:1], v[4:5]
	v_pk_add_f32 v[4:5], v[2:3], v[166:167]
	v_pk_add_f32 v[2:3], v[0:1], v[168:169]
	v_mov_b32_e32 v0, v4
	v_pk_mul_f32 v[6:7], v[2:3], v[2:3]
	v_mov_b32_e32 v1, v2
	v_mov_b32_e32 v2, v5
	v_pk_fma_f32 v[4:5], v[4:5], v[4:5], v[6:7]
	s_addk_i32 s23, 0x80
	s_add_i32 s12, s12, s34
	s_and_b32 s98, s17, 1
	s_lshl_b32 s98, s98, 12
	s_lshl_b32 s99, s28, 2
	s_add_i32 s98, s98, s99
	s_add_i32 s98, s98, s20
	s_addk_i32 s98, 0x1c00
	v_mbcnt_lo_u32_b32 v6, -1, 0
	v_mbcnt_hi_u32_b32 v6, -1, v6
	v_lshl_add_u32 v6, v6, 4, s98
	ds_write_b128 v6, v[0:3]
	global_load_dword v241, v[164:165], off
	s_cmpk_eq_i32 s28, 0x400
	v_add_u32_e32 v177, 0x200, v177
	v_add_f32_e32 v0, v4, v5
	s_waitcnt vmcnt(1)
	v_mov_b32_e32 v149, v202
	v_mov_b32_e32 v150, v203
	v_mov_b32_e32 v151, v204
	v_mov_b32_e32 v143, v198
	v_mov_b32_e32 v144, v199
	v_mov_b32_e32 v145, v200
	v_mov_b32_e32 v131, v156
	v_mov_b32_e32 v132, v157
	v_mov_b32_e32 v133, v158
	v_mov_b32_e32 v137, v152
	v_mov_b32_e32 v138, v153
	v_mov_b32_e32 v139, v154
	s_waitcnt lgkmcnt(0)
	v_add_f32_e32 v0, v155, v0
	ds_write_b32 v178, v0
	s_cbranch_scc0 .LBB0_3403
	s_bitcmp1_b32 s17, 0
	s_cbranch_scc0 .Lp12_noflush
	v_mbcnt_lo_u32_b32 v0, -1, 0
	v_mbcnt_hi_u32_b32 v0, -1, v0
	v_lshl_add_u32 v1, v0, 4, s20
	v_and_b32_e32 v2, 15, v0
	v_lshrrev_b32_e32 v3, 4, v0
	v_lshlrev_b32_e32 v2, 6, v2
	v_lshl_add_u32 v2, v3, 4, v2
	s_lshl_b32 s98, s17, 10
	s_add_i32 s98, s98, 0xfffffc00
	v_add_u32_e32 v2, s98, v2
	ds_read_b128 v[4:7], v1 offset:8192
	ds_read_b128 v[8:11], v1 offset:12288
	ds_read_b128 v[12:15], v1 offset:9216
	ds_read_b128 v[16:19], v1 offset:13312
	ds_read_b128 v[20:23], v1 offset:10240
	ds_read_b128 v[24:27], v1 offset:14336
	ds_read_b128 v[28:31], v1 offset:11264
	ds_read_b128 v[32:35], v1 offset:15360
	s_mul_i32 s98, s34, 0
	s_add_i32 s98, s98, s94
	s_lshl_b32 s98, s98, 14
	s_add_u32 s98, s26, s98
	s_addc_u32 s99, s27, 0
	s_waitcnt lgkmcnt(6)
	global_store_dwordx4 v2, v[4:7], s[98:99]
	global_store_dwordx4 v2, v[8:11], s[98:99] offset:1024
	s_mul_i32 s100, s34, 1
	s_add_i32 s100, s100, s94
	s_lshl_b32 s100, s100, 14
	s_add_u32 s100, s26, s100
	s_addc_u32 s101, s27, 0
	s_waitcnt lgkmcnt(4)
	global_store_dwordx4 v2, v[12:15], s[100:101]
	global_store_dwordx4 v2, v[16:19], s[100:101] offset:1024
	s_mul_i32 s98, s34, 2
	s_add_i32 s98, s98, s94
	s_lshl_b32 s98, s98, 14
	s_add_u32 s98, s26, s98
	s_addc_u32 s99, s27, 0
	s_waitcnt lgkmcnt(2)
	global_store_dwordx4 v2, v[20:23], s[98:99]
	global_store_dwordx4 v2, v[24:27], s[98:99] offset:1024
	s_mul_i32 s100, s34, 3
	s_add_i32 s100, s100, s94
	s_lshl_b32 s100, s100, 14
	s_add_u32 s100, s26, s100
	s_addc_u32 s101, s27, 0
	s_waitcnt lgkmcnt(0)
	global_store_dwordx4 v2, v[28:31], s[100:101]
	global_store_dwordx4 v2, v[32:35], s[100:101] offset:1024
; __device__ __forceinline__ int fresh_lane() { int l; asm volatile("v_mbcnt_lo_u32_b32 %0, -1, 0\n\tv_mbcnt_hi_u32_b32 %0, -1, %0" : "=v"(l)); return l; }
; __device__ __forceinline__ float wave_sum(float v) { v = dpp_add16(v); return (rdlane(v, 0) + rdlane(v, 16)) + (rdlane(v, 32) + rdlane(v, 48)); }
; __device__ __forceinline__ void p12_peer(Frame& F) {
;     ...
;       __builtin_amdgcn_fence(__ATOMIC_SEQ_CST, "agent");
;       const int l2_ = fresh_lane(), lo2_ = 16 * (l2_ & 15) + 4 * (l2_ >> 4);
; #pragma unroll
;       for (int i = 0; i < 4; ++i) { const int t = F.gw + i * F.NGW;
;           const float rs = 1.0f / sqrtf(wave_sum(SSQ[i * 64 + l2_]) * (1.f / D_) + 1e-6f);
; _Pragma("nounroll")
;           for (int c0 = 0; c0 < 16; c0 += 8) {
; #pragma unroll
;               for (int c = c0; c < c0 + 8; ++c) { const size_t col = (size_t)t * D_ + (size_t)(unsigned)(256 * c + lo2_); const f32x4 gn = *(const f32x4*)(lnf + (256 * c + lo2_));
;                   const f32x4 o = *(const f32x4*)(F.out + col);
.Lp12_noflush:
	s_cmp_eq_u32 s19, 16
	s_mov_b32 s17, s19
	s_cbranch_scc0 .LBB0_3402
	s_waitcnt vmcnt(0) lgkmcnt(0)
	buffer_inv sc1
	v_mbcnt_lo_u32_b32 v0, -1, 0
	v_mbcnt_hi_u32_b32 v0, -1, v0
	v_lshl_add_u32 v7, v0, 2, s20
	v_and_b32_e32 v2, 15, v0
	v_lshrrev_b32_e32 v3, 4, v0
	v_lshlrev_b32_e32 v2, 6, v2
	v_lshl_add_u32 v6, v3, 4, v2
	v_add_u32_e32 v10, 0x1000, v6
	v_add_u32_e32 v11, 0x2000, v6
	v_add_u32_e32 v12, 0x3000, v6
	s_lshl_b64 s[0:1], s[94:95], 14
	s_add_u32 s12, s26, s0
	s_addc_u32 s13, s27, s1
	s_lshl_b64 s[0:1], s[4:5], 14
	s_add_u32 s14, s26, s0
	s_addc_u32 s15, s27, s1
	s_lshl_b64 s[0:1], s[8:9], 14
	s_add_u32 s16, s26, s0
	s_addc_u32 s17, s27, s1
	s_lshl_b64 s[0:1], s[10:11], 14
	s_add_u32 s18, s26, s0
	s_addc_u32 s19, s27, s1
	global_load_dwordx4 v[60:63], v6, s[24:25] offset:0
	global_load_dwordx4 v[64:67], v6, s[24:25] offset:1024
	global_load_dwordx4 v[68:71], v6, s[24:25] offset:2048
	global_load_dwordx4 v[72:75], v6, s[24:25] offset:3072
	global_load_dwordx4 v[76:79], v10, s[24:25] offset:0
	global_load_dwordx4 v[80:83], v10, s[24:25] offset:1024
	global_load_dwordx4 v[84:87], v10, s[24:25] offset:2048
	global_load_dwordx4 v[88:91], v10, s[24:25] offset:3072
	global_load_dwordx4 v[92:95], v11, s[24:25] offset:0
	global_load_dwordx4 v[96:99], v11, s[24:25] offset:1024
	global_load_dwordx4 v[100:103], v11, s[24:25] offset:2048
	global_load_dwordx4 v[104:107], v11, s[24:25] offset:3072
	global_load_dwordx4 v[108:111], v12, s[24:25] offset:0
	global_load_dwordx4 v[112:115], v12, s[24:25] offset:1024
	global_load_dwordx4 v[116:119], v12, s[24:25] offset:2048
	global_load_dwordx4 v[120:123], v12, s[24:25] offset:3072
	global_load_dwordx4 v[124:127], v6, s[12:13] offset:0
	global_load_dwordx4 v[128:131], v6, s[12:13] offset:1024
	global_load_dwordx4 v[132:135], v6, s[12:13] offset:2048
	global_load_dwordx4 v[136:139], v6, s[12:13] offset:3072
	global_load_dwordx4 v[140:143], v10, s[12:13] offset:0
	global_load_dwordx4 v[144:147], v10, s[12:13] offset:1024
	global_load_dwordx4 v[148:151], v10, s[12:13] offset:2048
	global_load_dwordx4 v[152:155], v10, s[12:13] offset:3072
	global_load_dwordx4 v[156:159], v11, s[12:13] offset:0
	global_load_dwordx4 v[160:163], v11, s[12:13] offset:1024
	global_load_dwordx4 v[164:167], v11, s[12:13] offset:2048
	global_load_dwordx4 v[168:171], v11, s[12:13] offset:3072
	global_load_dwordx4 v[172:175], v12, s[12:13] offset:0
	global_load_dwordx4 v[176:179], v12, s[12:13] offset:1024
	global_load_dwordx4 v[180:183], v12, s[12:13] offset:2048
	global_load_dwordx4 v[184:187], v12, s[12:13] offset:3072
	global_load_dwordx4 v[188:191], v6, s[14:15] offset:0
	global_load_dwordx4 v[192:195], v6, s[14:15] offset:1024
	global_load_dwordx4 v[196:199], v6, s[14:15] offset:2048
	global_load_dwordx4 v[200:203], v6, s[14:15] offset:3072
	global_load_dwordx4 v[204:207], v10, s[14:15] offset:0
	global_load_dwordx4 v[208:211], v10, s[14:15] offset:1024
	global_load_dwordx4 v[212:215], v10, s[14:15] offset:2048
	global_load_dwordx4 v[216:219], v10, s[14:15] offset:3072
	global_load_dwordx4 v[220:223], v11, s[14:15] offset:0
	global_load_dwordx4 v[224:227], v11, s[14:15] offset:1024
	global_load_dwordx4 v[228:231], v11, s[14:15] offset:2048
	global_load_dwordx4 v[232:235], v11, s[14:15] offset:3072
	global_load_dwordx4 v[236:239], v12, s[14:15] offset:0
	global_load_dwordx4 v[240:243], v12, s[14:15] offset:1024
	global_load_dwordx4 v[244:247], v12, s[14:15] offset:2048
	global_load_dwordx4 v[248:251], v12, s[14:15] offset:3072
	ds_read_b32 v1, v7 offset:4096
	s_waitcnt lgkmcnt(0)
	v_add_f32_dpp v1, v1, v1 quad_perm:[1,0,3,2] row_mask:0xf bank_mask:0xf bound_ctrl:1
	s_nop 1
	v_add_f32_dpp v1, v1, v1 quad_perm:[2,3,0,1] row_mask:0xf bank_mask:0xf bound_ctrl:1
	s_nop 1
	v_add_f32_dpp v1, v1, v1 row_half_mirror row_mask:0xf bank_mask:0xf bound_ctrl:1
	s_nop 1
	v_add_f32_dpp v1, v1, v1 row_mirror row_mask:0xf bank_mask:0xf bound_ctrl:1
	s_nop 0
	v_readlane_b32 s1, v1, 16
	v_readlane_b32 s0, v1, 0
	s_nop 0
	v_mov_b32_e32 v3, s1
	v_readlane_b32 s1, v1, 48
	v_add_f32_e32 v3, s0, v3
	v_readlane_b32 s0, v1, 32
	v_mov_b32_e32 v1, s1
	s_nop 0
	v_add_f32_e32 v1, s0, v1
	v_add_f32_e32 v1, v3, v1
	v_mov_b32_e32 v3, 0x358637bd
	v_fmac_f32_e32 v3, 0x39800000, v1
	s_mov_b32 s0, 0xf800000
	v_mul_f32_e32 v1, 0x4f800000, v3
	v_cmp_gt_f32_e32 vcc, s0, v3
	s_nop 1
	v_cndmask_b32_e32 v1, v3, v1, vcc
	v_sqrt_f32_e32 v3, v1
	s_nop 0
	v_add_u32_e32 v4, -1, v3
	v_fma_f32 v5, -v4, v3, v1
	v_cmp_ge_f32_e64 s[0:1], 0, v5
	v_add_u32_e32 v5, 1, v3
	s_nop 0
	v_cndmask_b32_e64 v4, v3, v4, s[0:1]
	v_fma_f32 v3, -v5, v3, v1
	v_cmp_lt_f32_e64 s[0:1], 0, v3
	s_nop 1
	v_cndmask_b32_e64 v3, v4, v5, s[0:1]
	v_mul_f32_e32 v4, 0x37800000, v3
	v_cndmask_b32_e32 v3, v3, v4, vcc
	v_mov_b32_e32 v4, 0x260
	v_cmp_class_f32_e32 vcc, v1, v4
	s_nop 1
	v_cndmask_b32_e32 v3, v3, v1, vcc
	v_div_scale_f32 v4, s[0:1], v3, v3, 1.0
	v_rcp_f32_e32 v5, v4
	s_nop 0
	v_fma_f32 v0, -v4, v5, 1.0
	v_fmac_f32_e32 v5, v0, v5
	v_div_scale_f32 v0, vcc, 1.0, v3, 1.0
	v_mul_f32_e32 v2, v0, v5
	v_fma_f32 v8, -v4, v2, v0
	v_fmac_f32_e32 v2, v8, v5
	v_fma_f32 v0, -v4, v2, v0
	v_div_fmas_f32 v0, v0, v5, v2
	v_div_fixup_f32 v2, v0, v3, 1.0
	v_mov_b32_e32 v40, v2
	v_mov_b32_e32 v41, v2
	ds_read_b32 v1, v7 offset:4352
	s_waitcnt lgkmcnt(0)
; __device__ __forceinline__ int fresh_lane() { int l; asm volatile("v_mbcnt_lo_u32_b32 %0, -1, 0\n\tv_mbcnt_hi_u32_b32 %0, -1, %0" : "=v"(l)); return l; }
; __device__ __forceinline__ float wave_sum(float v) { v = dpp_add16(v); return (rdlane(v, 0) + rdlane(v, 16)) + (rdlane(v, 32) + rdlane(v, 48)); }
; __device__ __forceinline__ void p12_peer(Frame& F) {
;     ...
;       const int l2_ = fresh_lane(), lo2_ = 16 * (l2_ & 15) + 4 * (l2_ >> 4);
; #pragma unroll
;       for (int i = 0; i < 4; ++i) { const int t = F.gw + i * F.NGW;
;           const float rs = 1.0f / sqrtf(wave_sum(SSQ[i * 64 + l2_]) * (1.f / D_) + 1e-6f);
; _Pragma("nounroll")
;           for (int c0 = 0; c0 < 16; c0 += 8) {
; #pragma unroll
;               for (int c = c0; c < c0 + 8; ++c) { const size_t col = (size_t)t * D_ + (size_t)(unsigned)(256 * c + lo2_); const f32x4 gn = *(const f32x4*)(lnf + (256 * c + lo2_));
;                   const f32x4 o = *(const f32x4*)(F.out + col);
;                   *(f32x4*)(F.out + col) = (f32x4){o.x * rs * gn.x, o.y * rs * gn.y, o.z * rs * gn.z, o.w * rs * gn.w}; }
;               asm volatile("" ::: "memory"); } }
	v_add_f32_dpp v1, v1, v1 quad_perm:[1,0,3,2] row_mask:0xf bank_mask:0xf bound_ctrl:1
	s_nop 1
	v_add_f32_dpp v1, v1, v1 quad_perm:[2,3,0,1] row_mask:0xf bank_mask:0xf bound_ctrl:1
	s_nop 1
	v_add_f32_dpp v1, v1, v1 row_half_mirror row_mask:0xf bank_mask:0xf bound_ctrl:1
	s_nop 1
	v_add_f32_dpp v1, v1, v1 row_mirror row_mask:0xf bank_mask:0xf bound_ctrl:1
	s_nop 0
	v_readlane_b32 s1, v1, 16
	v_readlane_b32 s0, v1, 0
	s_nop 0
	v_mov_b32_e32 v3, s1
	v_readlane_b32 s1, v1, 48
	v_add_f32_e32 v3, s0, v3
	v_readlane_b32 s0, v1, 32
	v_mov_b32_e32 v1, s1
	s_nop 0
	v_add_f32_e32 v1, s0, v1
	v_add_f32_e32 v1, v3, v1
	v_mov_b32_e32 v3, 0x358637bd
	v_fmac_f32_e32 v3, 0x39800000, v1
	s_mov_b32 s0, 0xf800000
	v_mul_f32_e32 v1, 0x4f800000, v3
	v_cmp_gt_f32_e32 vcc, s0, v3
	s_nop 1
	v_cndmask_b32_e32 v1, v3, v1, vcc
	v_sqrt_f32_e32 v3, v1
	s_nop 0
	v_add_u32_e32 v4, -1, v3
	v_fma_f32 v5, -v4, v3, v1
	v_cmp_ge_f32_e64 s[0:1], 0, v5
	v_add_u32_e32 v5, 1, v3
	s_nop 0
	v_cndmask_b32_e64 v4, v3, v4, s[0:1]
	v_fma_f32 v3, -v5, v3, v1
	v_cmp_lt_f32_e64 s[0:1], 0, v3
	s_nop 1
	v_cndmask_b32_e64 v3, v4, v5, s[0:1]
	v_mul_f32_e32 v4, 0x37800000, v3
	v_cndmask_b32_e32 v3, v3, v4, vcc
	v_mov_b32_e32 v4, 0x260
	v_cmp_class_f32_e32 vcc, v1, v4
	s_nop 1
	v_cndmask_b32_e32 v3, v3, v1, vcc
	v_div_scale_f32 v4, s[0:1], v3, v3, 1.0
	v_rcp_f32_e32 v5, v4
	s_nop 0
	v_fma_f32 v0, -v4, v5, 1.0
	v_fmac_f32_e32 v5, v0, v5
	v_div_scale_f32 v0, vcc, 1.0, v3, 1.0
	v_mul_f32_e32 v2, v0, v5
	v_fma_f32 v8, -v4, v2, v0
	v_fmac_f32_e32 v2, v8, v5
	v_fma_f32 v0, -v4, v2, v0
	v_div_fmas_f32 v0, v0, v5, v2
	v_div_fixup_f32 v2, v0, v3, 1.0
	v_mov_b32_e32 v42, v2
	v_mov_b32_e32 v43, v2
	ds_read_b32 v1, v7 offset:4608
	s_waitcnt lgkmcnt(0)
	v_add_f32_dpp v1, v1, v1 quad_perm:[1,0,3,2] row_mask:0xf bank_mask:0xf bound_ctrl:1
	s_nop 1
	v_add_f32_dpp v1, v1, v1 quad_perm:[2,3,0,1] row_mask:0xf bank_mask:0xf bound_ctrl:1
	s_nop 1
	v_add_f32_dpp v1, v1, v1 row_half_mirror row_mask:0xf bank_mask:0xf bound_ctrl:1
	s_nop 1
	v_add_f32_dpp v1, v1, v1 row_mirror row_mask:0xf bank_mask:0xf bound_ctrl:1
	s_nop 0
	v_readlane_b32 s1, v1, 16
	v_readlane_b32 s0, v1, 0
	s_nop 0
	v_mov_b32_e32 v3, s1
	v_readlane_b32 s1, v1, 48
	v_add_f32_e32 v3, s0, v3
	v_readlane_b32 s0, v1, 32
	v_mov_b32_e32 v1, s1
	s_nop 0
	v_add_f32_e32 v1, s0, v1
	v_add_f32_e32 v1, v3, v1
	v_mov_b32_e32 v3, 0x358637bd
	v_fmac_f32_e32 v3, 0x39800000, v1
	s_mov_b32 s0, 0xf800000
	v_mul_f32_e32 v1, 0x4f800000, v3
	v_cmp_gt_f32_e32 vcc, s0, v3
	s_nop 1
	v_cndmask_b32_e32 v1, v3, v1, vcc
	v_sqrt_f32_e32 v3, v1
	s_nop 0
	v_add_u32_e32 v4, -1, v3
	v_fma_f32 v5, -v4, v3, v1
	v_cmp_ge_f32_e64 s[0:1], 0, v5
	v_add_u32_e32 v5, 1, v3
	s_nop 0
	v_cndmask_b32_e64 v4, v3, v4, s[0:1]
	v_fma_f32 v3, -v5, v3, v1
	v_cmp_lt_f32_e64 s[0:1], 0, v3
	s_nop 1
	v_cndmask_b32_e64 v3, v4, v5, s[0:1]
	v_mul_f32_e32 v4, 0x37800000, v3
	v_cndmask_b32_e32 v3, v3, v4, vcc
	v_mov_b32_e32 v4, 0x260
	v_cmp_class_f32_e32 vcc, v1, v4
	s_nop 1
	v_cndmask_b32_e32 v3, v3, v1, vcc
	v_div_scale_f32 v4, s[0:1], v3, v3, 1.0
	v_rcp_f32_e32 v5, v4
	s_nop 0
	v_fma_f32 v0, -v4, v5, 1.0
	v_fmac_f32_e32 v5, v0, v5
	v_div_scale_f32 v0, vcc, 1.0, v3, 1.0
	v_mul_f32_e32 v2, v0, v5
	v_fma_f32 v8, -v4, v2, v0
	v_fmac_f32_e32 v2, v8, v5
	v_fma_f32 v0, -v4, v2, v0
	v_div_fmas_f32 v0, v0, v5, v2
	v_div_fixup_f32 v2, v0, v3, 1.0
	v_mov_b32_e32 v44, v2
	v_mov_b32_e32 v45, v2
	ds_read_b32 v1, v7 offset:4864
	s_waitcnt lgkmcnt(0)
	v_add_f32_dpp v1, v1, v1 quad_perm:[1,0,3,2] row_mask:0xf bank_mask:0xf bound_ctrl:1
	s_nop 1
	v_add_f32_dpp v1, v1, v1 quad_perm:[2,3,0,1] row_mask:0xf bank_mask:0xf bound_ctrl:1
	s_nop 1
	v_add_f32_dpp v1, v1, v1 row_half_mirror row_mask:0xf bank_mask:0xf bound_ctrl:1
	s_nop 1
	v_add_f32_dpp v1, v1, v1 row_mirror row_mask:0xf bank_mask:0xf bound_ctrl:1
	s_nop 0
	v_readlane_b32 s1, v1, 16
	v_readlane_b32 s0, v1, 0
	s_nop 0
	v_mov_b32_e32 v3, s1
	v_readlane_b32 s1, v1, 48
	v_add_f32_e32 v3, s0, v3
	v_readlane_b32 s0, v1, 32
	v_mov_b32_e32 v1, s1
	s_nop 0
	v_add_f32_e32 v1, s0, v1
	v_add_f32_e32 v1, v3, v1
	v_mov_b32_e32 v3, 0x358637bd
	v_fmac_f32_e32 v3, 0x39800000, v1
	s_mov_b32 s0, 0xf800000
	v_mul_f32_e32 v1, 0x4f800000, v3
	v_cmp_gt_f32_e32 vcc, s0, v3
	s_nop 1
	v_cndmask_b32_e32 v1, v3, v1, vcc
	v_sqrt_f32_e32 v3, v1
	s_nop 0
	v_add_u32_e32 v4, -1, v3
	v_fma_f32 v5, -v4, v3, v1
	v_cmp_ge_f32_e64 s[0:1], 0, v5
	v_add_u32_e32 v5, 1, v3
	s_nop 0
	v_cndmask_b32_e64 v4, v3, v4, s[0:1]
	v_fma_f32 v3, -v5, v3, v1
	v_cmp_lt_f32_e64 s[0:1], 0, v3
	s_nop 1
	v_cndmask_b32_e64 v3, v4, v5, s[0:1]
	v_mul_f32_e32 v4, 0x37800000, v3
	v_cndmask_b32_e32 v3, v3, v4, vcc
	v_mov_b32_e32 v4, 0x260
	v_cmp_class_f32_e32 vcc, v1, v4
	s_nop 1
	v_cndmask_b32_e32 v3, v3, v1, vcc
	v_div_scale_f32 v4, s[0:1], v3, v3, 1.0
	v_rcp_f32_e32 v5, v4
	s_nop 0
	v_fma_f32 v0, -v4, v5, 1.0
	v_fmac_f32_e32 v5, v0, v5
	v_div_scale_f32 v0, vcc, 1.0, v3, 1.0
	v_mul_f32_e32 v2, v0, v5
	v_fma_f32 v8, -v4, v2, v0
	v_fmac_f32_e32 v2, v8, v5
	v_fma_f32 v0, -v4, v2, v0
	v_div_fmas_f32 v0, v0, v5, v2
	v_div_fixup_f32 v2, v0, v3, 1.0
	v_mov_b32_e32 v46, v2
	v_mov_b32_e32 v47, v2
	s_waitcnt vmcnt(31)
	v_pk_mul_f32 v[124:125], v[40:41], v[124:125]
	v_pk_mul_f32 v[126:127], v[40:41], v[126:127]
	v_pk_mul_f32 v[124:125], v[60:61], v[124:125]
	v_pk_mul_f32 v[126:127], v[62:63], v[126:127]
	global_store_dwordx4 v6, v[124:127], s[12:13] offset:0
	s_waitcnt vmcnt(31)
	v_pk_mul_f32 v[128:129], v[40:41], v[128:129]
	v_pk_mul_f32 v[130:131], v[40:41], v[130:131]
	v_pk_mul_f32 v[128:129], v[64:65], v[128:129]
	v_pk_mul_f32 v[130:131], v[66:67], v[130:131]
	global_store_dwordx4 v6, v[128:131], s[12:13] offset:1024
	s_waitcnt vmcnt(31)
; __device__ __forceinline__ int fresh_lane() { int l; asm volatile("v_mbcnt_lo_u32_b32 %0, -1, 0\n\tv_mbcnt_hi_u32_b32 %0, -1, %0" : "=v"(l)); return l; }
; __device__ __forceinline__ float wave_sum(float v) { v = dpp_add16(v); return (rdlane(v, 0) + rdlane(v, 16)) + (rdlane(v, 32) + rdlane(v, 48)); }
; __device__ __forceinline__ void p12_peer(Frame& F) {
;     ...
;       const int l2_ = fresh_lane(), lo2_ = 16 * (l2_ & 15) + 4 * (l2_ >> 4);
; #pragma unroll
;       for (int i = 0; i < 4; ++i) { const int t = F.gw + i * F.NGW;
;           const float rs = 1.0f / sqrtf(wave_sum(SSQ[i * 64 + l2_]) * (1.f / D_) + 1e-6f);
; _Pragma("nounroll")
;           for (int c0 = 0; c0 < 16; c0 += 8) {
; #pragma unroll
;               for (int c = c0; c < c0 + 8; ++c) { const size_t col = (size_t)t * D_ + (size_t)(unsigned)(256 * c + lo2_); const f32x4 gn = *(const f32x4*)(lnf + (256 * c + lo2_));
;                   const f32x4 o = *(const f32x4*)(F.out + col);
;                   *(f32x4*)(F.out + col) = (f32x4){o.x * rs * gn.x, o.y * rs * gn.y, o.z * rs * gn.z, o.w * rs * gn.w}; }
;               asm volatile("" ::: "memory"); } }
	v_pk_mul_f32 v[132:133], v[40:41], v[132:133]
	v_pk_mul_f32 v[134:135], v[40:41], v[134:135]
	v_pk_mul_f32 v[132:133], v[68:69], v[132:133]
	v_pk_mul_f32 v[134:135], v[70:71], v[134:135]
	global_store_dwordx4 v6, v[132:135], s[12:13] offset:2048
	s_waitcnt vmcnt(31)
	v_pk_mul_f32 v[136:137], v[40:41], v[136:137]
	v_pk_mul_f32 v[138:139], v[40:41], v[138:139]
	v_pk_mul_f32 v[136:137], v[72:73], v[136:137]
	v_pk_mul_f32 v[138:139], v[74:75], v[138:139]
	global_store_dwordx4 v6, v[136:139], s[12:13] offset:3072
	s_waitcnt vmcnt(31)
	v_pk_mul_f32 v[140:141], v[40:41], v[140:141]
	v_pk_mul_f32 v[142:143], v[40:41], v[142:143]
	v_pk_mul_f32 v[140:141], v[76:77], v[140:141]
	v_pk_mul_f32 v[142:143], v[78:79], v[142:143]
	global_store_dwordx4 v10, v[140:143], s[12:13] offset:0
	s_waitcnt vmcnt(31)
	v_pk_mul_f32 v[144:145], v[40:41], v[144:145]
	v_pk_mul_f32 v[146:147], v[40:41], v[146:147]
	v_pk_mul_f32 v[144:145], v[80:81], v[144:145]
	v_pk_mul_f32 v[146:147], v[82:83], v[146:147]
	global_store_dwordx4 v10, v[144:147], s[12:13] offset:1024
	s_waitcnt vmcnt(31)
	v_pk_mul_f32 v[148:149], v[40:41], v[148:149]
	v_pk_mul_f32 v[150:151], v[40:41], v[150:151]
	v_pk_mul_f32 v[148:149], v[84:85], v[148:149]
	v_pk_mul_f32 v[150:151], v[86:87], v[150:151]
	global_store_dwordx4 v10, v[148:151], s[12:13] offset:2048
	s_waitcnt vmcnt(31)
	v_pk_mul_f32 v[152:153], v[40:41], v[152:153]
	v_pk_mul_f32 v[154:155], v[40:41], v[154:155]
	v_pk_mul_f32 v[152:153], v[88:89], v[152:153]
	v_pk_mul_f32 v[154:155], v[90:91], v[154:155]
	global_store_dwordx4 v10, v[152:155], s[12:13] offset:3072
	s_waitcnt vmcnt(31)
	v_pk_mul_f32 v[156:157], v[40:41], v[156:157]
	v_pk_mul_f32 v[158:159], v[40:41], v[158:159]
	v_pk_mul_f32 v[156:157], v[92:93], v[156:157]
	v_pk_mul_f32 v[158:159], v[94:95], v[158:159]
	global_store_dwordx4 v11, v[156:159], s[12:13] offset:0
	s_waitcnt vmcnt(31)
	v_pk_mul_f32 v[160:161], v[40:41], v[160:161]
	v_pk_mul_f32 v[162:163], v[40:41], v[162:163]
	v_pk_mul_f32 v[160:161], v[96:97], v[160:161]
	v_pk_mul_f32 v[162:163], v[98:99], v[162:163]
	global_store_dwordx4 v11, v[160:163], s[12:13] offset:1024
	s_waitcnt vmcnt(31)
	v_pk_mul_f32 v[164:165], v[40:41], v[164:165]
	v_pk_mul_f32 v[166:167], v[40:41], v[166:167]
	v_pk_mul_f32 v[164:165], v[100:101], v[164:165]
	v_pk_mul_f32 v[166:167], v[102:103], v[166:167]
	global_store_dwordx4 v11, v[164:167], s[12:13] offset:2048
	s_waitcnt vmcnt(31)
	v_pk_mul_f32 v[168:169], v[40:41], v[168:169]
	v_pk_mul_f32 v[170:171], v[40:41], v[170:171]
	v_pk_mul_f32 v[168:169], v[104:105], v[168:169]
	v_pk_mul_f32 v[170:171], v[106:107], v[170:171]
	global_store_dwordx4 v11, v[168:171], s[12:13] offset:3072
	s_waitcnt vmcnt(31)
	v_pk_mul_f32 v[172:173], v[40:41], v[172:173]
	v_pk_mul_f32 v[174:175], v[40:41], v[174:175]
	v_pk_mul_f32 v[172:173], v[108:109], v[172:173]
	v_pk_mul_f32 v[174:175], v[110:111], v[174:175]
	global_store_dwordx4 v12, v[172:175], s[12:13] offset:0
	s_waitcnt vmcnt(31)
	v_pk_mul_f32 v[176:177], v[40:41], v[176:177]
	v_pk_mul_f32 v[178:179], v[40:41], v[178:179]
	v_pk_mul_f32 v[176:177], v[112:113], v[176:177]
	v_pk_mul_f32 v[178:179], v[114:115], v[178:179]
	global_store_dwordx4 v12, v[176:179], s[12:13] offset:1024
	s_waitcnt vmcnt(31)
	v_pk_mul_f32 v[180:181], v[40:41], v[180:181]
	v_pk_mul_f32 v[182:183], v[40:41], v[182:183]
	v_pk_mul_f32 v[180:181], v[116:117], v[180:181]
	v_pk_mul_f32 v[182:183], v[118:119], v[182:183]
	global_store_dwordx4 v12, v[180:183], s[12:13] offset:2048
	s_waitcnt vmcnt(31)
	v_pk_mul_f32 v[184:185], v[40:41], v[184:185]
	v_pk_mul_f32 v[186:187], v[40:41], v[186:187]
	v_pk_mul_f32 v[184:185], v[120:121], v[184:185]
	v_pk_mul_f32 v[186:187], v[122:123], v[186:187]
	global_store_dwordx4 v12, v[184:187], s[12:13] offset:3072
	s_nop 1
	global_load_dwordx4 v[124:127], v6, s[16:17] offset:0
	global_load_dwordx4 v[128:131], v6, s[16:17] offset:1024
	global_load_dwordx4 v[132:135], v6, s[16:17] offset:2048
	global_load_dwordx4 v[136:139], v6, s[16:17] offset:3072
	global_load_dwordx4 v[140:143], v10, s[16:17] offset:0
	global_load_dwordx4 v[144:147], v10, s[16:17] offset:1024
	global_load_dwordx4 v[148:151], v10, s[16:17] offset:2048
	global_load_dwordx4 v[152:155], v10, s[16:17] offset:3072
	global_load_dwordx4 v[156:159], v11, s[16:17] offset:0
	global_load_dwordx4 v[160:163], v11, s[16:17] offset:1024
	global_load_dwordx4 v[164:167], v11, s[16:17] offset:2048
	global_load_dwordx4 v[168:171], v11, s[16:17] offset:3072
	global_load_dwordx4 v[172:175], v12, s[16:17] offset:0
	global_load_dwordx4 v[176:179], v12, s[16:17] offset:1024
	global_load_dwordx4 v[180:183], v12, s[16:17] offset:2048
	global_load_dwordx4 v[184:187], v12, s[16:17] offset:3072
	s_waitcnt vmcnt(47)
	v_pk_mul_f32 v[188:189], v[42:43], v[188:189]
	v_pk_mul_f32 v[190:191], v[42:43], v[190:191]
	v_pk_mul_f32 v[188:189], v[60:61], v[188:189]
	v_pk_mul_f32 v[190:191], v[62:63], v[190:191]
	global_store_dwordx4 v6, v[188:191], s[14:15] offset:0
	s_waitcnt vmcnt(47)
	v_pk_mul_f32 v[192:193], v[42:43], v[192:193]
	v_pk_mul_f32 v[194:195], v[42:43], v[194:195]
	v_pk_mul_f32 v[192:193], v[64:65], v[192:193]
	v_pk_mul_f32 v[194:195], v[66:67], v[194:195]
	global_store_dwordx4 v6, v[192:195], s[14:15] offset:1024
	s_waitcnt vmcnt(47)
	v_pk_mul_f32 v[196:197], v[42:43], v[196:197]
	v_pk_mul_f32 v[198:199], v[42:43], v[198:199]
	v_pk_mul_f32 v[196:197], v[68:69], v[196:197]
	v_pk_mul_f32 v[198:199], v[70:71], v[198:199]
	global_store_dwordx4 v6, v[196:199], s[14:15] offset:2048
	s_waitcnt vmcnt(47)
; __device__ __forceinline__ int fresh_lane() { int l; asm volatile("v_mbcnt_lo_u32_b32 %0, -1, 0\n\tv_mbcnt_hi_u32_b32 %0, -1, %0" : "=v"(l)); return l; }
; __device__ __forceinline__ float wave_sum(float v) { v = dpp_add16(v); return (rdlane(v, 0) + rdlane(v, 16)) + (rdlane(v, 32) + rdlane(v, 48)); }
; __device__ __forceinline__ void p12_peer(Frame& F) {
;     ...
;       const int l2_ = fresh_lane(), lo2_ = 16 * (l2_ & 15) + 4 * (l2_ >> 4);
; #pragma unroll
;       for (int i = 0; i < 4; ++i) { const int t = F.gw + i * F.NGW;
;           const float rs = 1.0f / sqrtf(wave_sum(SSQ[i * 64 + l2_]) * (1.f / D_) + 1e-6f);
; _Pragma("nounroll")
;           for (int c0 = 0; c0 < 16; c0 += 8) {
; #pragma unroll
;               for (int c = c0; c < c0 + 8; ++c) { const size_t col = (size_t)t * D_ + (size_t)(unsigned)(256 * c + lo2_); const f32x4 gn = *(const f32x4*)(lnf + (256 * c + lo2_));
;                   const f32x4 o = *(const f32x4*)(F.out + col);
;                   *(f32x4*)(F.out + col) = (f32x4){o.x * rs * gn.x, o.y * rs * gn.y, o.z * rs * gn.z, o.w * rs * gn.w}; }
;               asm volatile("" ::: "memory"); } }
	v_pk_mul_f32 v[200:201], v[42:43], v[200:201]
	v_pk_mul_f32 v[202:203], v[42:43], v[202:203]
	v_pk_mul_f32 v[200:201], v[72:73], v[200:201]
	v_pk_mul_f32 v[202:203], v[74:75], v[202:203]
	global_store_dwordx4 v6, v[200:203], s[14:15] offset:3072
	s_waitcnt vmcnt(47)
	v_pk_mul_f32 v[204:205], v[42:43], v[204:205]
	v_pk_mul_f32 v[206:207], v[42:43], v[206:207]
	v_pk_mul_f32 v[204:205], v[76:77], v[204:205]
	v_pk_mul_f32 v[206:207], v[78:79], v[206:207]
	global_store_dwordx4 v10, v[204:207], s[14:15] offset:0
	s_waitcnt vmcnt(47)
	v_pk_mul_f32 v[208:209], v[42:43], v[208:209]
	v_pk_mul_f32 v[210:211], v[42:43], v[210:211]
	v_pk_mul_f32 v[208:209], v[80:81], v[208:209]
	v_pk_mul_f32 v[210:211], v[82:83], v[210:211]
	global_store_dwordx4 v10, v[208:211], s[14:15] offset:1024
	s_waitcnt vmcnt(47)
	v_pk_mul_f32 v[212:213], v[42:43], v[212:213]
	v_pk_mul_f32 v[214:215], v[42:43], v[214:215]
	v_pk_mul_f32 v[212:213], v[84:85], v[212:213]
	v_pk_mul_f32 v[214:215], v[86:87], v[214:215]
	global_store_dwordx4 v10, v[212:215], s[14:15] offset:2048
	s_waitcnt vmcnt(47)
	v_pk_mul_f32 v[216:217], v[42:43], v[216:217]
	v_pk_mul_f32 v[218:219], v[42:43], v[218:219]
	v_pk_mul_f32 v[216:217], v[88:89], v[216:217]
	v_pk_mul_f32 v[218:219], v[90:91], v[218:219]
	global_store_dwordx4 v10, v[216:219], s[14:15] offset:3072
	s_waitcnt vmcnt(47)
	v_pk_mul_f32 v[220:221], v[42:43], v[220:221]
	v_pk_mul_f32 v[222:223], v[42:43], v[222:223]
	v_pk_mul_f32 v[220:221], v[92:93], v[220:221]
	v_pk_mul_f32 v[222:223], v[94:95], v[222:223]
	global_store_dwordx4 v11, v[220:223], s[14:15] offset:0
	s_waitcnt vmcnt(47)
	v_pk_mul_f32 v[224:225], v[42:43], v[224:225]
	v_pk_mul_f32 v[226:227], v[42:43], v[226:227]
	v_pk_mul_f32 v[224:225], v[96:97], v[224:225]
	v_pk_mul_f32 v[226:227], v[98:99], v[226:227]
	global_store_dwordx4 v11, v[224:227], s[14:15] offset:1024
	s_waitcnt vmcnt(47)
	v_pk_mul_f32 v[228:229], v[42:43], v[228:229]
	v_pk_mul_f32 v[230:231], v[42:43], v[230:231]
	v_pk_mul_f32 v[228:229], v[100:101], v[228:229]
	v_pk_mul_f32 v[230:231], v[102:103], v[230:231]
	global_store_dwordx4 v11, v[228:231], s[14:15] offset:2048
	s_waitcnt vmcnt(47)
	v_pk_mul_f32 v[232:233], v[42:43], v[232:233]
	v_pk_mul_f32 v[234:235], v[42:43], v[234:235]
	v_pk_mul_f32 v[232:233], v[104:105], v[232:233]
	v_pk_mul_f32 v[234:235], v[106:107], v[234:235]
	global_store_dwordx4 v11, v[232:235], s[14:15] offset:3072
	s_waitcnt vmcnt(47)
	v_pk_mul_f32 v[236:237], v[42:43], v[236:237]
	v_pk_mul_f32 v[238:239], v[42:43], v[238:239]
	v_pk_mul_f32 v[236:237], v[108:109], v[236:237]
	v_pk_mul_f32 v[238:239], v[110:111], v[238:239]
	global_store_dwordx4 v12, v[236:239], s[14:15] offset:0
	s_waitcnt vmcnt(47)
	v_pk_mul_f32 v[240:241], v[42:43], v[240:241]
	v_pk_mul_f32 v[242:243], v[42:43], v[242:243]
	v_pk_mul_f32 v[240:241], v[112:113], v[240:241]
	v_pk_mul_f32 v[242:243], v[114:115], v[242:243]
	global_store_dwordx4 v12, v[240:243], s[14:15] offset:1024
	s_waitcnt vmcnt(47)
	v_pk_mul_f32 v[244:245], v[42:43], v[244:245]
	v_pk_mul_f32 v[246:247], v[42:43], v[246:247]
	v_pk_mul_f32 v[244:245], v[116:117], v[244:245]
	v_pk_mul_f32 v[246:247], v[118:119], v[246:247]
	global_store_dwordx4 v12, v[244:247], s[14:15] offset:2048
	s_waitcnt vmcnt(47)
	v_pk_mul_f32 v[248:249], v[42:43], v[248:249]
	v_pk_mul_f32 v[250:251], v[42:43], v[250:251]
	v_pk_mul_f32 v[248:249], v[120:121], v[248:249]
	v_pk_mul_f32 v[250:251], v[122:123], v[250:251]
	global_store_dwordx4 v12, v[248:251], s[14:15] offset:3072
	s_nop 1
	global_load_dwordx4 v[188:191], v6, s[18:19] offset:0
	global_load_dwordx4 v[192:195], v6, s[18:19] offset:1024
	global_load_dwordx4 v[196:199], v6, s[18:19] offset:2048
	global_load_dwordx4 v[200:203], v6, s[18:19] offset:3072
	global_load_dwordx4 v[204:207], v10, s[18:19] offset:0
	global_load_dwordx4 v[208:211], v10, s[18:19] offset:1024
	global_load_dwordx4 v[212:215], v10, s[18:19] offset:2048
	global_load_dwordx4 v[216:219], v10, s[18:19] offset:3072
	global_load_dwordx4 v[220:223], v11, s[18:19] offset:0
	global_load_dwordx4 v[224:227], v11, s[18:19] offset:1024
	global_load_dwordx4 v[228:231], v11, s[18:19] offset:2048
	global_load_dwordx4 v[232:235], v11, s[18:19] offset:3072
	global_load_dwordx4 v[236:239], v12, s[18:19] offset:0
	global_load_dwordx4 v[240:243], v12, s[18:19] offset:1024
	global_load_dwordx4 v[244:247], v12, s[18:19] offset:2048
	global_load_dwordx4 v[248:251], v12, s[18:19] offset:3072
	s_waitcnt vmcnt(47)
	v_pk_mul_f32 v[124:125], v[44:45], v[124:125]
	v_pk_mul_f32 v[126:127], v[44:45], v[126:127]
	v_pk_mul_f32 v[124:125], v[60:61], v[124:125]
	v_pk_mul_f32 v[126:127], v[62:63], v[126:127]
	global_store_dwordx4 v6, v[124:127], s[16:17] offset:0
	s_waitcnt vmcnt(47)
	v_pk_mul_f32 v[128:129], v[44:45], v[128:129]
	v_pk_mul_f32 v[130:131], v[44:45], v[130:131]
	v_pk_mul_f32 v[128:129], v[64:65], v[128:129]
	v_pk_mul_f32 v[130:131], v[66:67], v[130:131]
	global_store_dwordx4 v6, v[128:131], s[16:17] offset:1024
	s_waitcnt vmcnt(47)
	v_pk_mul_f32 v[132:133], v[44:45], v[132:133]
	v_pk_mul_f32 v[134:135], v[44:45], v[134:135]
	v_pk_mul_f32 v[132:133], v[68:69], v[132:133]
	v_pk_mul_f32 v[134:135], v[70:71], v[134:135]
	global_store_dwordx4 v6, v[132:135], s[16:17] offset:2048
	s_waitcnt vmcnt(47)
	v_pk_mul_f32 v[136:137], v[44:45], v[136:137]
	v_pk_mul_f32 v[138:139], v[44:45], v[138:139]
	v_pk_mul_f32 v[136:137], v[72:73], v[136:137]
	v_pk_mul_f32 v[138:139], v[74:75], v[138:139]
	global_store_dwordx4 v6, v[136:139], s[16:17] offset:3072
	s_waitcnt vmcnt(47)
; __device__ __forceinline__ int fresh_lane() { int l; asm volatile("v_mbcnt_lo_u32_b32 %0, -1, 0\n\tv_mbcnt_hi_u32_b32 %0, -1, %0" : "=v"(l)); return l; }
; __device__ __forceinline__ float wave_sum(float v) { v = dpp_add16(v); return (rdlane(v, 0) + rdlane(v, 16)) + (rdlane(v, 32) + rdlane(v, 48)); }
; __device__ __forceinline__ void p12_peer(Frame& F) {
;     ...
;       const int l2_ = fresh_lane(), lo2_ = 16 * (l2_ & 15) + 4 * (l2_ >> 4);
; #pragma unroll
;       for (int i = 0; i < 4; ++i) { const int t = F.gw + i * F.NGW;
;           const float rs = 1.0f / sqrtf(wave_sum(SSQ[i * 64 + l2_]) * (1.f / D_) + 1e-6f);
; _Pragma("nounroll")
;           for (int c0 = 0; c0 < 16; c0 += 8) {
; #pragma unroll
;               for (int c = c0; c < c0 + 8; ++c) { const size_t col = (size_t)t * D_ + (size_t)(unsigned)(256 * c + lo2_); const f32x4 gn = *(const f32x4*)(lnf + (256 * c + lo2_));
;                   const f32x4 o = *(const f32x4*)(F.out + col);
;                   *(f32x4*)(F.out + col) = (f32x4){o.x * rs * gn.x, o.y * rs * gn.y, o.z * rs * gn.z, o.w * rs * gn.w}; }
;               asm volatile("" ::: "memory"); } }
	v_pk_mul_f32 v[140:141], v[44:45], v[140:141]
	v_pk_mul_f32 v[142:143], v[44:45], v[142:143]
	v_pk_mul_f32 v[140:141], v[76:77], v[140:141]
	v_pk_mul_f32 v[142:143], v[78:79], v[142:143]
	global_store_dwordx4 v10, v[140:143], s[16:17] offset:0
	s_waitcnt vmcnt(47)
	v_pk_mul_f32 v[144:145], v[44:45], v[144:145]
	v_pk_mul_f32 v[146:147], v[44:45], v[146:147]
	v_pk_mul_f32 v[144:145], v[80:81], v[144:145]
	v_pk_mul_f32 v[146:147], v[82:83], v[146:147]
	global_store_dwordx4 v10, v[144:147], s[16:17] offset:1024
	s_waitcnt vmcnt(47)
	v_pk_mul_f32 v[148:149], v[44:45], v[148:149]
	v_pk_mul_f32 v[150:151], v[44:45], v[150:151]
	v_pk_mul_f32 v[148:149], v[84:85], v[148:149]
	v_pk_mul_f32 v[150:151], v[86:87], v[150:151]
	global_store_dwordx4 v10, v[148:151], s[16:17] offset:2048
	s_waitcnt vmcnt(47)
	v_pk_mul_f32 v[152:153], v[44:45], v[152:153]
	v_pk_mul_f32 v[154:155], v[44:45], v[154:155]
	v_pk_mul_f32 v[152:153], v[88:89], v[152:153]
	v_pk_mul_f32 v[154:155], v[90:91], v[154:155]
	global_store_dwordx4 v10, v[152:155], s[16:17] offset:3072
	s_waitcnt vmcnt(47)
	v_pk_mul_f32 v[156:157], v[44:45], v[156:157]
	v_pk_mul_f32 v[158:159], v[44:45], v[158:159]
	v_pk_mul_f32 v[156:157], v[92:93], v[156:157]
	v_pk_mul_f32 v[158:159], v[94:95], v[158:159]
	global_store_dwordx4 v11, v[156:159], s[16:17] offset:0
	s_waitcnt vmcnt(47)
	v_pk_mul_f32 v[160:161], v[44:45], v[160:161]
	v_pk_mul_f32 v[162:163], v[44:45], v[162:163]
	v_pk_mul_f32 v[160:161], v[96:97], v[160:161]
	v_pk_mul_f32 v[162:163], v[98:99], v[162:163]
	global_store_dwordx4 v11, v[160:163], s[16:17] offset:1024
	s_waitcnt vmcnt(47)
	v_pk_mul_f32 v[164:165], v[44:45], v[164:165]
	v_pk_mul_f32 v[166:167], v[44:45], v[166:167]
	v_pk_mul_f32 v[164:165], v[100:101], v[164:165]
	v_pk_mul_f32 v[166:167], v[102:103], v[166:167]
	global_store_dwordx4 v11, v[164:167], s[16:17] offset:2048
	s_waitcnt vmcnt(47)
	v_pk_mul_f32 v[168:169], v[44:45], v[168:169]
	v_pk_mul_f32 v[170:171], v[44:45], v[170:171]
	v_pk_mul_f32 v[168:169], v[104:105], v[168:169]
	v_pk_mul_f32 v[170:171], v[106:107], v[170:171]
	global_store_dwordx4 v11, v[168:171], s[16:17] offset:3072
	s_waitcnt vmcnt(47)
	v_pk_mul_f32 v[172:173], v[44:45], v[172:173]
	v_pk_mul_f32 v[174:175], v[44:45], v[174:175]
	v_pk_mul_f32 v[172:173], v[108:109], v[172:173]
	v_pk_mul_f32 v[174:175], v[110:111], v[174:175]
	global_store_dwordx4 v12, v[172:175], s[16:17] offset:0
	s_waitcnt vmcnt(47)
	v_pk_mul_f32 v[176:177], v[44:45], v[176:177]
	v_pk_mul_f32 v[178:179], v[44:45], v[178:179]
	v_pk_mul_f32 v[176:177], v[112:113], v[176:177]
	v_pk_mul_f32 v[178:179], v[114:115], v[178:179]
	global_store_dwordx4 v12, v[176:179], s[16:17] offset:1024
	s_waitcnt vmcnt(47)
	v_pk_mul_f32 v[180:181], v[44:45], v[180:181]
	v_pk_mul_f32 v[182:183], v[44:45], v[182:183]
	v_pk_mul_f32 v[180:181], v[116:117], v[180:181]
	v_pk_mul_f32 v[182:183], v[118:119], v[182:183]
	global_store_dwordx4 v12, v[180:183], s[16:17] offset:2048
	s_waitcnt vmcnt(47)
	v_pk_mul_f32 v[184:185], v[44:45], v[184:185]
	v_pk_mul_f32 v[186:187], v[44:45], v[186:187]
	v_pk_mul_f32 v[184:185], v[120:121], v[184:185]
	v_pk_mul_f32 v[186:187], v[122:123], v[186:187]
	global_store_dwordx4 v12, v[184:187], s[16:17] offset:3072
	s_waitcnt vmcnt(31)
	v_pk_mul_f32 v[188:189], v[46:47], v[188:189]
	v_pk_mul_f32 v[190:191], v[46:47], v[190:191]
	v_pk_mul_f32 v[188:189], v[60:61], v[188:189]
	v_pk_mul_f32 v[190:191], v[62:63], v[190:191]
	global_store_dwordx4 v6, v[188:191], s[18:19] offset:0
	s_waitcnt vmcnt(31)
	v_pk_mul_f32 v[192:193], v[46:47], v[192:193]
	v_pk_mul_f32 v[194:195], v[46:47], v[194:195]
	v_pk_mul_f32 v[192:193], v[64:65], v[192:193]
	v_pk_mul_f32 v[194:195], v[66:67], v[194:195]
	global_store_dwordx4 v6, v[192:195], s[18:19] offset:1024
	s_waitcnt vmcnt(31)
; __device__ __forceinline__ int fresh_lane() { int l; asm volatile("v_mbcnt_lo_u32_b32 %0, -1, 0\n\tv_mbcnt_hi_u32_b32 %0, -1, %0" : "=v"(l)); return l; }
; __device__ __forceinline__ float wave_sum(float v) { v = dpp_add16(v); return (rdlane(v, 0) + rdlane(v, 16)) + (rdlane(v, 32) + rdlane(v, 48)); }
; __device__ __forceinline__ void p12_peer(Frame& F) {
;     ...
;       const int l2_ = fresh_lane(), lo2_ = 16 * (l2_ & 15) + 4 * (l2_ >> 4);
; #pragma unroll
;       for (int i = 0; i < 4; ++i) { const int t = F.gw + i * F.NGW;
;           const float rs = 1.0f / sqrtf(wave_sum(SSQ[i * 64 + l2_]) * (1.f / D_) + 1e-6f);
; _Pragma("nounroll")
;           for (int c0 = 0; c0 < 16; c0 += 8) {
; #pragma unroll
;               for (int c = c0; c < c0 + 8; ++c) { const size_t col = (size_t)t * D_ + (size_t)(unsigned)(256 * c + lo2_); const f32x4 gn = *(const f32x4*)(lnf + (256 * c + lo2_));
;                   const f32x4 o = *(const f32x4*)(F.out + col);
;                   *(f32x4*)(F.out + col) = (f32x4){o.x * rs * gn.x, o.y * rs * gn.y, o.z * rs * gn.z, o.w * rs * gn.w}; }
;               asm volatile("" ::: "memory"); } }
	v_pk_mul_f32 v[196:197], v[46:47], v[196:197]
	v_pk_mul_f32 v[198:199], v[46:47], v[198:199]
	v_pk_mul_f32 v[196:197], v[68:69], v[196:197]
	v_pk_mul_f32 v[198:199], v[70:71], v[198:199]
	global_store_dwordx4 v6, v[196:199], s[18:19] offset:2048
	s_waitcnt vmcnt(31)
	v_pk_mul_f32 v[200:201], v[46:47], v[200:201]
	v_pk_mul_f32 v[202:203], v[46:47], v[202:203]
	v_pk_mul_f32 v[200:201], v[72:73], v[200:201]
	v_pk_mul_f32 v[202:203], v[74:75], v[202:203]
	global_store_dwordx4 v6, v[200:203], s[18:19] offset:3072
	s_waitcnt vmcnt(31)
	v_pk_mul_f32 v[204:205], v[46:47], v[204:205]
	v_pk_mul_f32 v[206:207], v[46:47], v[206:207]
	v_pk_mul_f32 v[204:205], v[76:77], v[204:205]
	v_pk_mul_f32 v[206:207], v[78:79], v[206:207]
	global_store_dwordx4 v10, v[204:207], s[18:19] offset:0
	s_waitcnt vmcnt(31)
	v_pk_mul_f32 v[208:209], v[46:47], v[208:209]
	v_pk_mul_f32 v[210:211], v[46:47], v[210:211]
	v_pk_mul_f32 v[208:209], v[80:81], v[208:209]
	v_pk_mul_f32 v[210:211], v[82:83], v[210:211]
	global_store_dwordx4 v10, v[208:211], s[18:19] offset:1024
	s_waitcnt vmcnt(31)
	v_pk_mul_f32 v[212:213], v[46:47], v[212:213]
	v_pk_mul_f32 v[214:215], v[46:47], v[214:215]
	v_pk_mul_f32 v[212:213], v[84:85], v[212:213]
	v_pk_mul_f32 v[214:215], v[86:87], v[214:215]
	global_store_dwordx4 v10, v[212:215], s[18:19] offset:2048
	s_waitcnt vmcnt(31)
	v_pk_mul_f32 v[216:217], v[46:47], v[216:217]
	v_pk_mul_f32 v[218:219], v[46:47], v[218:219]
	v_pk_mul_f32 v[216:217], v[88:89], v[216:217]
	v_pk_mul_f32 v[218:219], v[90:91], v[218:219]
	global_store_dwordx4 v10, v[216:219], s[18:19] offset:3072
	s_waitcnt vmcnt(31)
	v_pk_mul_f32 v[220:221], v[46:47], v[220:221]
	v_pk_mul_f32 v[222:223], v[46:47], v[222:223]
	v_pk_mul_f32 v[220:221], v[92:93], v[220:221]
	v_pk_mul_f32 v[222:223], v[94:95], v[222:223]
	global_store_dwordx4 v11, v[220:223], s[18:19] offset:0
	s_waitcnt vmcnt(31)
	v_pk_mul_f32 v[224:225], v[46:47], v[224:225]
	v_pk_mul_f32 v[226:227], v[46:47], v[226:227]
	v_pk_mul_f32 v[224:225], v[96:97], v[224:225]
	v_pk_mul_f32 v[226:227], v[98:99], v[226:227]
	global_store_dwordx4 v11, v[224:227], s[18:19] offset:1024
	s_waitcnt vmcnt(31)
	v_pk_mul_f32 v[228:229], v[46:47], v[228:229]
	v_pk_mul_f32 v[230:231], v[46:47], v[230:231]
	v_pk_mul_f32 v[228:229], v[100:101], v[228:229]
	v_pk_mul_f32 v[230:231], v[102:103], v[230:231]
	global_store_dwordx4 v11, v[228:231], s[18:19] offset:2048
	s_waitcnt vmcnt(31)
	v_pk_mul_f32 v[232:233], v[46:47], v[232:233]
	v_pk_mul_f32 v[234:235], v[46:47], v[234:235]
	v_pk_mul_f32 v[232:233], v[104:105], v[232:233]
	v_pk_mul_f32 v[234:235], v[106:107], v[234:235]
	global_store_dwordx4 v11, v[232:235], s[18:19] offset:3072
	s_waitcnt vmcnt(31)
	v_pk_mul_f32 v[236:237], v[46:47], v[236:237]
	v_pk_mul_f32 v[238:239], v[46:47], v[238:239]
	v_pk_mul_f32 v[236:237], v[108:109], v[236:237]
	v_pk_mul_f32 v[238:239], v[110:111], v[238:239]
	global_store_dwordx4 v12, v[236:239], s[18:19] offset:0
	s_waitcnt vmcnt(31)
	v_pk_mul_f32 v[240:241], v[46:47], v[240:241]
	v_pk_mul_f32 v[242:243], v[46:47], v[242:243]
	v_pk_mul_f32 v[240:241], v[112:113], v[240:241]
	v_pk_mul_f32 v[242:243], v[114:115], v[242:243]
	global_store_dwordx4 v12, v[240:243], s[18:19] offset:1024
	s_waitcnt vmcnt(31)
	v_pk_mul_f32 v[244:245], v[46:47], v[244:245]
	v_pk_mul_f32 v[246:247], v[46:47], v[246:247]
	v_pk_mul_f32 v[244:245], v[116:117], v[244:245]
	v_pk_mul_f32 v[246:247], v[118:119], v[246:247]
	global_store_dwordx4 v12, v[244:247], s[18:19] offset:2048
	s_waitcnt vmcnt(31)
	v_pk_mul_f32 v[248:249], v[46:47], v[248:249]
	v_pk_mul_f32 v[250:251], v[46:47], v[250:251]
	v_pk_mul_f32 v[248:249], v[120:121], v[248:249]
	v_pk_mul_f32 v[250:251], v[122:123], v[250:251]
	global_store_dwordx4 v12, v[248:251], s[18:19] offset:3072

; __global__ void __launch_bounds__(NWAVES * 64, 2) mk_fwd(Args args) {
	.amdhsa_kernel _Z6mk_fwd4Args
		.amdhsa_group_segment_fixed_size 0
		.amdhsa_private_segment_fixed_size 0
		.amdhsa_kernarg_size 472
		.amdhsa_user_sgpr_count 2
		.amdhsa_user_sgpr_dispatch_ptr 0
		.amdhsa_user_sgpr_queue_ptr 0
		.amdhsa_user_sgpr_kernarg_segment_ptr 1
		.amdhsa_user_sgpr_dispatch_id 0
		.amdhsa_user_sgpr_kernarg_preload_length 0
		.amdhsa_user_sgpr_kernarg_preload_offset 0
		.amdhsa_user_sgpr_private_segment_size 0
		.amdhsa_uses_dynamic_stack 0
		.amdhsa_enable_private_segment 0
		.amdhsa_system_sgpr_workgroup_id_x 1
		.amdhsa_system_sgpr_workgroup_id_y 0
		.amdhsa_system_sgpr_workgroup_id_z 0
		.amdhsa_system_sgpr_workgroup_info 0
		.amdhsa_system_vgpr_workitem_id 0
		.amdhsa_next_free_vgpr 255
		.amdhsa_next_free_sgpr 102
		.amdhsa_accum_offset 256
		.amdhsa_reserve_vcc 1
		.amdhsa_float_round_mode_32 0
		.amdhsa_float_round_mode_16_64 0
		.amdhsa_float_denorm_mode_32 3
		.amdhsa_float_denorm_mode_16_64 3
		.amdhsa_dx10_clamp 1
		.amdhsa_ieee_mode 1
		.amdhsa_fp16_overflow 0
		.amdhsa_tg_split 0
		.amdhsa_exception_fp_ieee_invalid_op 0
		.amdhsa_exception_fp_denorm_src 0
		.amdhsa_exception_fp_ieee_div_zero 0
		.amdhsa_exception_fp_ieee_overflow 0
		.amdhsa_exception_fp_ieee_underflow 0
		.amdhsa_exception_fp_ieee_inexact 0
		.amdhsa_exception_int_div_zero 0
	.end_amdhsa_kernel

; __global__ void __launch_bounds__(NWAVES * 64, 2) mk_fwd(Args args) {
amdhsa.kernels:
  - .agpr_count:     0
    .args:
      - .offset:         0
        .size:           216
        .value_kind:     by_value
      - .offset:         216
        .size:           4
        .value_kind:     hidden_block_count_x
      - .offset:         220
        .size:           4
        .value_kind:     hidden_block_count_y
      - .offset:         224
        .size:           4
        .value_kind:     hidden_block_count_z
      - .offset:         228
        .size:           2
        .value_kind:     hidden_group_size_x
      - .offset:         230
        .size:           2
        .value_kind:     hidden_group_size_y
      - .offset:         232
        .size:           2
        .value_kind:     hidden_group_size_z
      - .offset:         234
        .size:           2
        .value_kind:     hidden_remainder_x
      - .offset:         236
        .size:           2
        .value_kind:     hidden_remainder_y
      - .offset:         238
        .size:           2
        .value_kind:     hidden_remainder_z
      - .offset:         256
        .size:           8
        .value_kind:     hidden_global_offset_x
      - .offset:         264
        .size:           8
        .value_kind:     hidden_global_offset_y
      - .offset:         272
        .size:           8
        .value_kind:     hidden_global_offset_z
      - .offset:         280
        .size:           2
        .value_kind:     hidden_grid_dims
      - .offset:         336
        .size:           4
        .value_kind:     hidden_dynamic_lds_size
    .group_segment_fixed_size: 0
    .kernarg_segment_align: 8
    .kernarg_segment_size: 472
    .language:       OpenCL C
    .language_version:
      - 2
      - 0
    .max_flat_workgroup_size: 512
    .name:           _Z6mk_fwd4Args
    .private_segment_fixed_size: 0
    .sgpr_count:     108
    .sgpr_spill_count: 50
    .symbol:         _Z6mk_fwd4Args.kd
    .uniform_work_group_size: 1
    .uses_dynamic_stack: false
    .vgpr_count:     255
    .vgpr_spill_count: 0
    .wavefront_size: 64
